# last K block: bank fragments pre-loaded during the wait, 16 MFMAs back to back
# baseline (speedup 1.0000x reference)
_Z12fused_kernelPKfS0_Pf:
	s_load_dwordx4 s[12:15], s[0:1], 0x0
	s_load_dwordx2 s[8:9], s[0:1], 0x10
	s_lshl_b32 s0, s2, 5
	s_and_b32 s0, s0, 0xe0
	s_lshr_b32 s3, s2, 3
	s_add_i32 s0, s0, s3
	v_and_b32_e32 v1, 63, v0
	v_lshrrev_b32_e32 v200, 6, v0
	s_lshl_b32 s0, s0, 17
	v_lshlrev_b32_e32 v194, 4, v0
	v_lshl_add_u32 v2, v200, 25, s0
	v_lshlrev_b32_e32 v198, 4, v1
	v_add_u32_e32 v106, 0x2000, v194
	v_add_u32_e32 v107, 0x4000, v194
	v_or_b32_e32 v203, v2, v198
	v_lshlrev_b32_e32 v196, 10, v200
	v_mov_b32_e32 v195, 0
	v_or_b32_e32 v233, v203, v196
	s_mov_b32 s7, 0x20000
	s_brev_b32 s6, 8
	s_waitcnt lgkmcnt(0)
	s_and_b32 s5, s13, 0xffff
	s_mov_b32 s4, s12
	buffer_load_dwordx4 v[70:73], v233, s[4:7], 0 offen nt
	v_or_b32_e32 v227, 0x2000, v233
	buffer_load_dwordx4 v[66:69], v227, s[4:7], 0 offen nt
	v_or_b32_e32 v226, 0x4000, v233
	buffer_load_dwordx4 v[78:81], v226, s[4:7], 0 offen nt
	v_or_b32_e32 v227, 0x6000, v233
	buffer_load_dwordx4 v[74:77], v227, s[4:7], 0 offen nt
	v_or_b32_e32 v226, 0x8000, v233
	buffer_load_dwordx4 v[86:89], v226, s[4:7], 0 offen nt
	v_or_b32_e32 v227, 0xa000, v233
	buffer_load_dwordx4 v[82:85], v227, s[4:7], 0 offen nt
	v_or_b32_e32 v226, 0xc000, v233
	buffer_load_dwordx4 v[94:97], v226, s[4:7], 0 offen nt
	v_or_b32_e32 v227, 0xe000, v233
	buffer_load_dwordx4 v[90:93], v227, s[4:7], 0 offen nt
	v_or_b32_e32 v226, 0x10000, v233
	buffer_load_dwordx4 v[150:153], v226, s[4:7], 0 offen nt
	v_or_b32_e32 v227, 0x12000, v233
	buffer_load_dwordx4 v[146:149], v227, s[4:7], 0 offen nt
	v_or_b32_e32 v226, 0x14000, v233
	buffer_load_dwordx4 v[162:165], v226, s[4:7], 0 offen nt
	v_or_b32_e32 v227, 0x16000, v233
	buffer_load_dwordx4 v[154:157], v227, s[4:7], 0 offen nt
	v_or_b32_e32 v226, 0x18000, v233
	buffer_load_dwordx4 v[174:177], v226, s[4:7], 0 offen nt
	v_or_b32_e32 v227, 0x1a000, v233
	buffer_load_dwordx4 v[166:169], v227, s[4:7], 0 offen nt
	v_or_b32_e32 v226, 0x1c000, v233
	buffer_load_dwordx4 v[182:185], v226, s[4:7], 0 offen nt
	v_or_b32_e32 v227, 0x1e000, v233
	buffer_load_dwordx4 v[178:181], v227, s[4:7], 0 offen nt
	global_load_dwordx4 v[228:231], v194, s[14:15]
	global_load_dwordx4 v[98:101], v106, s[14:15]
	global_load_dwordx4 v[102:105], v107, s[14:15]
	v_add_u32_e32 v107, 0x6000, v194
	global_load_dwordx4 v[116:119], v107, s[14:15]
	v_add_u32_e32 v106, 0x8000, v194
	global_load_dwordx4 v[120:123], v106, s[14:15]
	v_add_u32_e32 v107, 0xa000, v194
	global_load_dwordx4 v[124:127], v107, s[14:15]
	v_add_u32_e32 v106, 0xc000, v194
	global_load_dwordx4 v[128:131], v106, s[14:15]
	v_add_u32_e32 v107, 0xe000, v194
	global_load_dwordx4 v[132:135], v107, s[14:15]
	v_add_u32_e32 v106, 0x10000, v194
	global_load_dwordx4 v[136:139], v106, s[14:15]
	v_add_u32_e32 v107, 0x12000, v194
	global_load_dwordx4 v[140:143], v107, s[14:15]
	v_add_u32_e32 v106, 0x14000, v194
	global_load_dwordx4 v[158:161], v106, s[14:15]
	v_add_u32_e32 v107, 0x16000, v194
	global_load_dwordx4 v[170:173], v107, s[14:15]
	v_add_u32_e32 v106, 0x18000, v194
	global_load_dwordx4 v[186:189], v106, s[14:15]
	v_add_u32_e32 v107, 0x1a000, v194
	global_load_dwordx4 v[190:193], v107, s[14:15]
	v_add_u32_e32 v106, 0x1c000, v194
	global_load_dwordx4 v[204:207], v106, s[14:15]
	v_add_u32_e32 v107, 0x1e000, v194
	global_load_dwordx4 v[208:211], v107, s[14:15]
	v_add_u32_e32 v106, 0x20000, v194
	global_load_dwordx4 v[212:215], v106, s[14:15]
	v_add_u32_e32 v107, 0x22000, v194
	global_load_dwordx4 v[216:219], v107, s[14:15]
	v_add_u32_e32 v106, 0x24000, v194
	global_load_dwordx4 v[220:223], v106, s[14:15]
	v_add_u32_e32 v107, 0x26000, v194
	global_load_dwordx4 v[112:115], v107, s[14:15]
	v_add_u32_e32 v224, 0x400, v196
	s_movk_i32 s0, 0x1c00
	v_and_or_b32 v224, v224, s0, v203
	buffer_load_dwordx4 v[62:65], v224, s[4:7], 0 offen nt
	v_or_b32_e32 v227, 0x2000, v224
	buffer_load_dwordx4 v[38:41], v227, s[4:7], 0 offen nt
	v_or_b32_e32 v226, 0x4000, v224
	buffer_load_dwordx4 v[42:45], v226, s[4:7], 0 offen nt
	v_or_b32_e32 v227, 0x6000, v224
	buffer_load_dwordx4 v[14:17], v227, s[4:7], 0 offen nt
	v_or_b32_e32 v226, 0x8000, v224
	buffer_load_dwordx4 v[46:49], v226, s[4:7], 0 offen nt
	v_or_b32_e32 v227, 0xa000, v224
	buffer_load_dwordx4 v[18:21], v227, s[4:7], 0 offen nt
	v_or_b32_e32 v226, 0xc000, v224
	buffer_load_dwordx4 v[50:53], v226, s[4:7], 0 offen nt
	v_or_b32_e32 v227, 0xe000, v224
	buffer_load_dwordx4 v[22:25], v227, s[4:7], 0 offen nt
	v_or_b32_e32 v226, 0x10000, v224
	buffer_load_dwordx4 v[54:57], v226, s[4:7], 0 offen nt
	v_or_b32_e32 v227, 0x12000, v224
	buffer_load_dwordx4 v[26:29], v227, s[4:7], 0 offen nt
	v_or_b32_e32 v226, 0x14000, v224
	buffer_load_dwordx4 v[58:61], v226, s[4:7], 0 offen nt
	v_or_b32_e32 v227, 0x16000, v224
	buffer_load_dwordx4 v[30:33], v227, s[4:7], 0 offen nt
	v_or_b32_e32 v226, 0x18000, v224
	buffer_load_dwordx4 v[34:37], v226, s[4:7], 0 offen nt
	v_or_b32_e32 v227, 0x1a000, v224
	buffer_load_dwordx4 v[6:9], v227, s[4:7], 0 offen nt
	v_or_b32_e32 v226, 0x1c000, v224
	buffer_load_dwordx4 v[10:13], v226, s[4:7], 0 offen nt
	v_or_b32_e32 v227, 0x1e000, v224
	buffer_load_dwordx4 v[2:5], v227, s[4:7], 0 offen nt
	s_mov_b32 s1, 0xe000
	s_mov_b32 s10, 0xa000
	s_mov_b32 s11, 0x6000
	s_mov_b32 s12, 0xc000
	s_mov_b32 s13, 0x8000
	s_mov_b32 s14, 0x1e000
	s_mov_b32 s15, 0x1c000
	s_mov_b32 s16, 0x2000
	s_mov_b32 s17, 0x4000
	s_mov_b32 s18, 0x10000
	s_mov_b32 s19, 0x1a000
	s_mov_b32 s20, 0x18000
	s_mov_b32 s21, 0x16000
	s_mov_b32 s22, 0x14000
	s_mov_b32 s23, 0x12000
	s_mov_b32 s24, 0xe0
	s_mov_b32 s26, 0x3e13bb63
	v_lshrrev_b32_e32 v144, 3, v0
	v_bfe_u32 v145, v0, 1, 2
	v_lshlrev_b32_e32 v108, 3, v0
	v_and_b32_e32 v109, 8, v108
	v_lshlrev_b32_e32 v224, 8, v144
	v_lshlrev_b32_e32 v225, 6, v145
	v_lshlrev_b32_e32 v226, 8, v145
	v_lshlrev_b32_e32 v110, 10, v144
	v_or3_b32 v110, v226, v110, v109
	v_or3_b32 v111, v224, v225, v109
	v_add_u32_e32 v111, 0xff00, v111
	v_add_u32_e32 v144, 0x24800, v194
	v_bfe_u32 v201, v0, 4, 2
	v_and_b32_e32 v197, 15, v0
	v_lshlrev_b32_e32 v202, 2, v201
	s_waitcnt vmcnt(34)
	v_pk_add_f32 v[224:225], v[228:229], 0 op_sel_hi:[1,0]
	v_pk_add_f32 v[226:227], v[230:231], 0 op_sel_hi:[1,0]
	v_cvt_pk_bf16_f32 v228, v228, v229
	v_cvt_pk_bf16_f32 v229, v230, v231
	v_pk_add_f32 v[224:225], v[224:225], v[98:99]
	v_pk_add_f32 v[226:227], v[226:227], v[100:101]
	v_cvt_pk_bf16_f32 v98, v98, v99
	v_cvt_pk_bf16_f32 v99, v100, v101
	ds_write2_b64 v110, v[228:229], v[98:99] offset1:2
	s_waitcnt vmcnt(32)
	v_pk_add_f32 v[224:225], v[224:225], v[102:103]
	v_pk_add_f32 v[226:227], v[226:227], v[104:105]
	v_cvt_pk_bf16_f32 v102, v102, v103
	v_cvt_pk_bf16_f32 v103, v104, v105
	v_pk_add_f32 v[224:225], v[224:225], v[116:117]
	v_pk_add_f32 v[226:227], v[226:227], v[118:119]
	v_cvt_pk_bf16_f32 v116, v116, v117
	v_cvt_pk_bf16_f32 v117, v118, v119
	ds_write2_b64 v110, v[102:103], v[116:117] offset0:4 offset1:6
	s_waitcnt vmcnt(30)
	v_pk_add_f32 v[224:225], v[224:225], v[120:121]
	v_pk_add_f32 v[226:227], v[226:227], v[122:123]
	v_cvt_pk_bf16_f32 v120, v120, v121
	v_cvt_pk_bf16_f32 v121, v122, v123
	v_pk_add_f32 v[224:225], v[224:225], v[124:125]
	v_pk_add_f32 v[226:227], v[226:227], v[126:127]
	v_cvt_pk_bf16_f32 v124, v124, v125
	v_cvt_pk_bf16_f32 v125, v126, v127
	ds_write2_b64 v110, v[120:121], v[124:125] offset0:8 offset1:10
	s_waitcnt vmcnt(28)
	v_pk_add_f32 v[224:225], v[224:225], v[128:129]
	v_pk_add_f32 v[226:227], v[226:227], v[130:131]
	v_cvt_pk_bf16_f32 v128, v128, v129
	v_cvt_pk_bf16_f32 v129, v130, v131
	v_pk_add_f32 v[224:225], v[224:225], v[132:133]
	v_pk_add_f32 v[226:227], v[226:227], v[134:135]
	v_cvt_pk_bf16_f32 v132, v132, v133
	v_cvt_pk_bf16_f32 v133, v134, v135
	ds_write2_b64 v110, v[128:129], v[132:133] offset0:12 offset1:14
	s_waitcnt vmcnt(26)
	v_pk_add_f32 v[224:225], v[224:225], v[136:137]
	v_pk_add_f32 v[226:227], v[226:227], v[138:139]
	v_cvt_pk_bf16_f32 v136, v136, v137
	v_cvt_pk_bf16_f32 v137, v138, v139
	v_pk_add_f32 v[224:225], v[224:225], v[140:141]
	v_pk_add_f32 v[226:227], v[226:227], v[142:143]
	v_cvt_pk_bf16_f32 v140, v140, v141
	v_cvt_pk_bf16_f32 v141, v142, v143
	ds_write2_b64 v110, v[136:137], v[140:141] offset0:16 offset1:18
	s_waitcnt vmcnt(24)
	v_pk_add_f32 v[224:225], v[224:225], v[158:159]
	v_pk_add_f32 v[226:227], v[226:227], v[160:161]
	v_cvt_pk_bf16_f32 v158, v158, v159
	v_cvt_pk_bf16_f32 v159, v160, v161
	v_pk_add_f32 v[224:225], v[224:225], v[170:171]
	v_pk_add_f32 v[226:227], v[226:227], v[172:173]
	v_cvt_pk_bf16_f32 v170, v170, v171
	v_cvt_pk_bf16_f32 v171, v172, v173
	ds_write2_b64 v110, v[158:159], v[170:171] offset0:20 offset1:22
	s_waitcnt vmcnt(22)
	v_pk_add_f32 v[224:225], v[224:225], v[186:187]
	v_pk_add_f32 v[226:227], v[226:227], v[188:189]
	v_cvt_pk_bf16_f32 v186, v186, v187
	v_cvt_pk_bf16_f32 v187, v188, v189
	v_pk_add_f32 v[224:225], v[224:225], v[190:191]
	v_pk_add_f32 v[226:227], v[226:227], v[192:193]
	v_cvt_pk_bf16_f32 v190, v190, v191
	v_cvt_pk_bf16_f32 v191, v192, v193
	ds_write2_b64 v110, v[186:187], v[190:191] offset0:24 offset1:26
	s_waitcnt vmcnt(20)
	v_pk_add_f32 v[224:225], v[224:225], v[204:205]
	v_pk_add_f32 v[226:227], v[226:227], v[206:207]
	v_cvt_pk_bf16_f32 v204, v204, v205
	v_cvt_pk_bf16_f32 v205, v206, v207
	v_pk_add_f32 v[224:225], v[224:225], v[208:209]
	v_pk_add_f32 v[226:227], v[226:227], v[210:211]
	v_cvt_pk_bf16_f32 v208, v208, v209
	v_cvt_pk_bf16_f32 v209, v210, v211
	ds_write2_b64 v110, v[204:205], v[208:209] offset0:28 offset1:30
	s_waitcnt vmcnt(18)
	v_pk_add_f32 v[224:225], v[224:225], v[212:213]
	v_pk_add_f32 v[226:227], v[226:227], v[214:215]
	v_cvt_pk_bf16_f32 v212, v212, v213
	v_cvt_pk_bf16_f32 v213, v214, v215
	v_pk_add_f32 v[224:225], v[224:225], v[216:217]
	v_pk_add_f32 v[226:227], v[226:227], v[218:219]
	v_cvt_pk_bf16_f32 v216, v216, v217
	v_cvt_pk_bf16_f32 v217, v218, v219
	ds_write2_b64 v111, v[212:213], v[216:217] offset0:32 offset1:34
	s_waitcnt vmcnt(16)
	v_pk_add_f32 v[224:225], v[224:225], v[220:221]
	v_pk_add_f32 v[226:227], v[226:227], v[222:223]
	v_cvt_pk_bf16_f32 v220, v220, v221
	v_cvt_pk_bf16_f32 v221, v222, v223
	v_pk_add_f32 v[224:225], v[224:225], v[112:113]
	v_pk_add_f32 v[226:227], v[226:227], v[114:115]
	v_cvt_pk_bf16_f32 v112, v112, v113
	v_cvt_pk_bf16_f32 v113, v114, v115
	ds_write2_b64 v111, v[220:221], v[112:113] offset0:36 offset1:38
	v_pk_mul_f32 v[224:225], v[224:225], s[26:27] op_sel_hi:[1,0]
	v_pk_mul_f32 v[226:227], v[226:227], s[26:27] op_sel_hi:[1,0]
	ds_write_b128 v144, v[224:227]
	v_and_or_b32 v98, v0, 3, v202
	v_mov_b32_e32 v99, 0x10000
	v_lshl_or_b32 v204, v98, 4, v99
	s_movk_i32 s25, 0x2100
	v_mov_b32_e32 v98, 0x14000
	v_mad_u32_u24 v199, v200, s25, v98
	v_add_u32_e32 v98, 0x800, v196
	v_and_or_b32 v186, v98, s0, v203
	v_or_b32_e32 v98, 0x2000, v186
	s_waitcnt lgkmcnt(0)
	s_barrier
	buffer_load_dwordx4 v[102:105], v186, s[4:7], 0 offen nt
	s_nop 0
	buffer_load_dwordx4 v[98:101], v98, s[4:7], 0 offen nt
	v_or_b32_e32 v106, 0x4000, v186
	v_or_b32_e32 v107, 0x6000, v186
	v_or_b32_e32 v114, 0x8000, v186
	v_or_b32_e32 v115, 0xa000, v186
	v_or_b32_e32 v122, 0xc000, v186
	v_or_b32_e32 v123, 0xe000, v186
	v_or_b32_e32 v130, 0x10000, v186
	v_or_b32_e32 v131, 0x12000, v186
	v_or_b32_e32 v138, 0x14000, v186
	v_or_b32_e32 v139, 0x16000, v186
	v_or_b32_e32 v158, 0x18000, v186
	v_or_b32_e32 v159, 0x1a000, v186
	v_or_b32_e32 v187, 0x1c000, v186
	v_or_b32_e32 v186, 0x1e000, v186
	v_or_b32_e32 v213, v199, v109
	v_and_b32_e32 v214, 0x1f0, v108
	buffer_load_dwordx4 v[110:113], v106, s[4:7], 0 offen nt
	s_nop 0
	buffer_load_dwordx4 v[106:109], v107, s[4:7], 0 offen nt
	s_nop 0
	buffer_load_dwordx4 v[118:121], v114, s[4:7], 0 offen nt
	s_nop 0
	buffer_load_dwordx4 v[114:117], v115, s[4:7], 0 offen nt
	s_nop 0
	buffer_load_dwordx4 v[126:129], v122, s[4:7], 0 offen nt
	s_nop 0
	buffer_load_dwordx4 v[122:125], v123, s[4:7], 0 offen nt
	s_nop 0
	buffer_load_dwordx4 v[134:137], v130, s[4:7], 0 offen nt
	s_nop 0
	buffer_load_dwordx4 v[130:133], v131, s[4:7], 0 offen nt
	s_nop 0
	buffer_load_dwordx4 v[142:145], v138, s[4:7], 0 offen nt
	s_nop 0
	buffer_load_dwordx4 v[138:141], v139, s[4:7], 0 offen nt
	s_nop 0
	buffer_load_dwordx4 v[170:173], v158, s[4:7], 0 offen nt
	s_nop 0
	buffer_load_dwordx4 v[158:161], v159, s[4:7], 0 offen nt
	s_nop 0
	buffer_load_dwordx4 v[190:193], v187, s[4:7], 0 offen nt
	s_nop 0
	buffer_load_dwordx4 v[186:189], v186, s[4:7], 0 offen nt
	s_waitcnt vmcnt(32)
	v_cvt_pk_bf16_f32 v66, v66, v67
	v_cvt_pk_bf16_f32 v67, v68, v69
	s_movk_i32 s25, 0x50
	v_xad_u32 v207, v214, s25, v213
	s_movk_i32 s25, 0x60
	v_xad_u32 v206, v214, s25, v213
	s_movk_i32 s25, 0x70
	v_xad_u32 v205, v214, s25, v213
	s_movk_i32 s25, 0x80
	v_xad_u32 v211, v214, 16, v213
	v_xad_u32 v231, v214, s25, v213
	s_movk_i32 s25, 0x90
	v_xad_u32 v210, v214, 32, v213
	v_xad_u32 v230, v214, s25, v213
	s_movk_i32 s25, 0xa0
	ds_write_b64 v211, v[66:67] offset:512
	v_cvt_pk_bf16_f32 v66, v78, v79
	v_cvt_pk_bf16_f32 v67, v80, v81
	v_xad_u32 v209, v214, 48, v213
	v_xad_u32 v229, v214, s25, v213
	s_movk_i32 s25, 0xb0
	ds_write_b64 v210, v[66:67] offset:1024
	v_cvt_pk_bf16_f32 v66, v74, v75
	v_cvt_pk_bf16_f32 v67, v76, v77
	v_xad_u32 v208, v214, 64, v213
	v_xad_u32 v228, v214, s25, v213
	s_movk_i32 s25, 0xc0
	ds_write_b64 v209, v[66:67] offset:1536
	v_cvt_pk_bf16_f32 v66, v86, v87
	v_cvt_pk_bf16_f32 v67, v88, v89
	v_xad_u32 v227, v214, s25, v213
	s_movk_i32 s25, 0xd0
	v_xad_u32 v225, v214, s24, v213
	s_movk_i32 s24, 0xf0
	ds_write_b64 v208, v[66:67] offset:2048
	v_cvt_pk_bf16_f32 v66, v82, v83
	v_cvt_pk_bf16_f32 v67, v84, v85
	v_add_u32_e32 v212, v213, v214
	v_xad_u32 v226, v214, s25, v213
	v_xad_u32 v224, v214, s24, v213
	v_lshl_add_u32 v213, v197, 9, v199
	v_bitop3_b32 v214, v201, v0, 15 bitop3:0x78
	ds_write_b64 v207, v[66:67] offset:2560
	v_cvt_pk_bf16_f32 v66, v94, v95
	v_cvt_pk_bf16_f32 v67, v96, v97
	v_lshl_or_b32 v223, v214, 4, v213
	v_bitop3_b32 v214, v201, v197, 4 bitop3:0x36
	ds_write_b64 v206, v[66:67] offset:3072
	v_cvt_pk_bf16_f32 v66, v90, v91
	v_cvt_pk_bf16_f32 v67, v92, v93
	v_lshl_or_b32 v222, v214, 4, v213
	v_bitop3_b32 v214, v201, v197, 8 bitop3:0x36
	ds_write_b64 v205, v[66:67] offset:3584
	v_cvt_pk_bf16_f32 v66, v150, v151
	v_cvt_pk_bf16_f32 v67, v152, v153
	v_lshl_or_b32 v221, v214, 4, v213
	v_bitop3_b32 v214, v201, v197, 12 bitop3:0x36
	ds_write_b64 v231, v[66:67] offset:4096
	v_cvt_pk_bf16_f32 v66, v146, v147
	v_cvt_pk_bf16_f32 v67, v148, v149
	v_lshl_or_b32 v219, v214, 4, v213
	v_bitop3_b32 v214, v201, v197, 16 bitop3:0x36
	ds_write_b64 v230, v[66:67] offset:4608
	v_cvt_pk_bf16_f32 v66, v162, v163
	v_cvt_pk_bf16_f32 v67, v164, v165
	v_lshl_add_u32 v218, v214, 4, v213
	v_bitop3_b32 v214, v201, v197, 20 bitop3:0x36
	ds_write_b64 v229, v[66:67] offset:5120
	v_cvt_pk_bf16_f32 v66, v154, v155
	v_cvt_pk_bf16_f32 v67, v156, v157
	v_lshl_add_u32 v217, v214, 4, v213
	v_bitop3_b32 v214, v201, v197, 24 bitop3:0x36
	ds_write_b64 v228, v[66:67] offset:5632
	v_cvt_pk_bf16_f32 v66, v174, v175
	v_cvt_pk_bf16_f32 v67, v176, v177
	v_lshl_add_u32 v216, v214, 4, v213
	v_bitop3_b32 v214, v201, v197, 28 bitop3:0x36
	ds_write_b64 v227, v[66:67] offset:6144
	v_cvt_pk_bf16_f32 v66, v166, v167
	v_cvt_pk_bf16_f32 v67, v168, v169
	v_add_u32_e32 v235, 3, v200
	v_lshl_add_u32 v213, v214, 4, v213
	ds_write_b64 v226, v[66:67] offset:6656
	v_cvt_pk_bf16_f32 v66, v182, v183
	v_cvt_pk_bf16_f32 v67, v184, v185
	v_cvt_pk_bf16_f32 v70, v70, v71
	v_cvt_pk_bf16_f32 v71, v72, v73
	ds_write_b64 v212, v[70:71]
	ds_write_b64 v225, v[66:67] offset:7168
	v_cvt_pk_bf16_f32 v66, v178, v179
	v_cvt_pk_bf16_f32 v67, v180, v181
	ds_write_b64 v224, v[66:67] offset:7680
	v_lshl_or_b32 v66, v200, 13, v198
	ds_read_b128 v[66:69], v66
	v_lshlrev_b32_e32 v220, 11, v200
	v_or_b32_e32 v70, v204, v220
	ds_read_b128 v[70:73], v70
	ds_read_b128 v[74:77], v223
	v_lshlrev_b32_e32 v232, 3, v200
	v_or_b32_e32 v214, 1, v232
	s_waitcnt lgkmcnt(0)
	v_mfma_f32_16x16x32_bf16 v[70:73], v[70:73], v[74:77], 0
	v_lshlrev_b32_e32 v215, 8, v214
	v_or_b32_e32 v78, v204, v215
	v_or_b32_e32 v184, 2, v232
	v_mfma_f32_16x16x32_bf16 v[66:69], v[66:69], v[74:77], 0
	v_lshl_or_b32 v74, v214, 10, v198
	ds_read_b128 v[74:77], v74
	ds_read_b128 v[78:81], v78
	ds_read_b128 v[82:85], v222
	v_lshlrev_b32_e32 v185, 8, v184
	s_waitcnt lgkmcnt(0)
	v_mfma_f32_16x16x32_bf16 v[70:73], v[78:81], v[82:85], v[70:73]
	v_or_b32_e32 v78, v204, v185
	v_or_b32_e32 v182, 3, v232
	v_lshlrev_b32_e32 v183, 8, v182
	v_mfma_f32_16x16x32_bf16 v[66:69], v[74:77], v[82:85], v[66:69]
	v_lshl_or_b32 v74, v184, 10, v198
	ds_read_b128 v[74:77], v74
	ds_read_b128 v[78:81], v78
	ds_read_b128 v[82:85], v221
	s_waitcnt lgkmcnt(0)
	v_mfma_f32_16x16x32_bf16 v[70:73], v[78:81], v[82:85], v[70:73]
	v_or_b32_e32 v78, v204, v183
	v_or_b32_e32 v180, 4, v232
	v_lshlrev_b32_e32 v181, 8, v180
	v_mfma_f32_16x16x32_bf16 v[66:69], v[74:77], v[82:85], v[66:69]
	v_lshl_or_b32 v74, v182, 10, v198
	ds_read_b128 v[74:77], v74
	ds_read_b128 v[78:81], v78
	ds_read_b128 v[82:85], v219
	s_waitcnt lgkmcnt(0)
	v_mfma_f32_16x16x32_bf16 v[66:69], v[74:77], v[82:85], v[66:69]
	v_lshl_or_b32 v74, v180, 10, v198
	ds_read_b128 v[74:77], v74
	v_or_b32_e32 v178, 5, v232
	v_mfma_f32_16x16x32_bf16 v[70:73], v[78:81], v[82:85], v[70:73]
	v_or_b32_e32 v78, v204, v181
	ds_read_b128 v[78:81], v78
	ds_read_b128 v[82:85], v218
	v_lshlrev_b32_e32 v179, 8, v178
	s_waitcnt lgkmcnt(0)
	v_mfma_f32_16x16x32_bf16 v[66:69], v[74:77], v[82:85], v[66:69]
	v_lshl_or_b32 v74, v178, 10, v198
	ds_read_b128 v[74:77], v74
	v_or_b32_e32 v176, 6, v232
	v_mfma_f32_16x16x32_bf16 v[70:73], v[78:81], v[82:85], v[70:73]
	v_or_b32_e32 v78, v204, v179
	ds_read_b128 v[78:81], v78
	ds_read_b128 v[82:85], v217
	v_lshlrev_b32_e32 v177, 8, v176
	s_waitcnt lgkmcnt(0)
	v_mfma_f32_16x16x32_bf16 v[66:69], v[74:77], v[82:85], v[66:69]
	v_lshl_or_b32 v74, v176, 10, v198
	ds_read_b128 v[74:77], v74
	v_or_b32_e32 v174, 7, v232
	v_mfma_f32_16x16x32_bf16 v[70:73], v[78:81], v[82:85], v[70:73]
	v_or_b32_e32 v78, v204, v177
	ds_read_b128 v[78:81], v78
	ds_read_b128 v[82:85], v216
	v_lshlrev_b32_e32 v175, 8, v174
	s_waitcnt lgkmcnt(0)
	v_mfma_f32_16x16x32_bf16 v[66:69], v[74:77], v[82:85], v[66:69]
	v_lshl_or_b32 v74, v174, 10, v198
	s_waitcnt vmcnt(16)
	v_cvt_pk_bf16_f32 v14, v14, v15
	v_cvt_pk_bf16_f32 v15, v16, v17
	v_mfma_f32_16x16x32_bf16 v[70:73], v[78:81], v[82:85], v[70:73]
	v_or_b32_e32 v78, v204, v175
	ds_read_b128 v[74:77], v74
	ds_read_b128 v[78:81], v78
	ds_read_b128 v[82:85], v213
	ds_write_b64 v209, v[14:15] offset:1536
	v_cvt_pk_bf16_f32 v14, v46, v47
	v_cvt_pk_bf16_f32 v15, v48, v49
	ds_write_b64 v208, v[14:15] offset:2048
	v_cvt_pk_bf16_f32 v14, v18, v19
	v_cvt_pk_bf16_f32 v15, v20, v21
	ds_write_b64 v207, v[14:15] offset:2560
	v_cvt_pk_bf16_f32 v14, v50, v51
	v_cvt_pk_bf16_f32 v15, v52, v53
	ds_write_b64 v206, v[14:15] offset:3072
	v_cvt_pk_bf16_f32 v14, v22, v23
	v_cvt_pk_bf16_f32 v15, v24, v25
	ds_write_b64 v205, v[14:15] offset:3584
	v_cvt_pk_bf16_f32 v14, v54, v55
	v_cvt_pk_bf16_f32 v15, v56, v57
	v_cvt_pk_bf16_f32 v6, v6, v7
	v_cvt_pk_bf16_f32 v2, v2, v3
	ds_write_b64 v231, v[14:15] offset:4096
	v_cvt_pk_bf16_f32 v14, v26, v27
	v_cvt_pk_bf16_f32 v15, v28, v29
	v_cvt_pk_bf16_f32 v7, v8, v9
	ds_write_b64 v226, v[6:7] offset:6656
	v_cvt_pk_bf16_f32 v6, v10, v11
	v_cvt_pk_bf16_f32 v3, v4, v5
	ds_write_b64 v224, v[2:3] offset:7680
	v_lshlrev_b32_e32 v2, 10, v235
	ds_write_b64 v230, v[14:15] offset:4608
	v_cvt_pk_bf16_f32 v14, v58, v59
	v_cvt_pk_bf16_f32 v15, v60, v61
	v_cvt_pk_bf16_f32 v7, v12, v13
	ds_write_b64 v225, v[6:7] offset:7168
	v_and_or_b32 v6, v2, s0, v203
	ds_write_b64 v229, v[14:15] offset:5120
	v_cvt_pk_bf16_f32 v14, v30, v31
	v_cvt_pk_bf16_f32 v15, v32, v33
	v_or_b32_e32 v7, 0x2000, v6
	ds_write_b64 v228, v[14:15] offset:5632
	v_cvt_pk_bf16_f32 v14, v34, v35
	v_cvt_pk_bf16_f32 v15, v36, v37
	buffer_load_dwordx4 v[2:5], v6, s[4:7], 0 offen nt
	buffer_load_dwordx4 v[10:13], v7, s[4:7], 0 offen nt
	v_or_b32_e32 v7, 0x4000, v6
	ds_write_b64 v227, v[14:15] offset:6144
	buffer_load_dwordx4 v[14:17], v7, s[4:7], 0 offen nt
	v_or_b32_e32 v7, 0x6000, v6
	v_cvt_pk_bf16_f32 v38, v38, v39
	v_cvt_pk_bf16_f32 v39, v40, v41
	buffer_load_dwordx4 v[22:25], v7, s[4:7], 0 offen nt
	v_or_b32_e32 v7, 0x8000, v6
	ds_write_b64 v211, v[38:39] offset:512
	v_cvt_pk_bf16_f32 v38, v42, v43
	v_cvt_pk_bf16_f32 v39, v44, v45
	buffer_load_dwordx4 v[30:33], v7, s[4:7], 0 offen nt
	v_or_b32_e32 v7, 0xa000, v6
	ds_write_b64 v210, v[38:39] offset:1024
	buffer_load_dwordx4 v[38:41], v7, s[4:7], 0 offen nt
	v_or_b32_e32 v7, 0xc000, v6
	buffer_load_dwordx4 v[46:49], v7, s[4:7], 0 offen nt
	v_or_b32_e32 v7, 0xe000, v6
	v_cvt_pk_bf16_f32 v62, v62, v63
	v_cvt_pk_bf16_f32 v63, v64, v65
	buffer_load_dwordx4 v[54:57], v7, s[4:7], 0 offen nt
	v_or_b32_e32 v7, 0x10000, v6
	ds_write_b64 v212, v[62:63]
	buffer_load_dwordx4 v[62:65], v7, s[4:7], 0 offen nt
	v_or_b32_e32 v7, 0x12000, v6
	s_waitcnt lgkmcnt(14)
	v_mfma_f32_16x16x32_bf16 v[66:69], v[74:77], v[82:85], v[66:69]
	v_mfma_f32_16x16x32_bf16 v[74:77], v[78:81], v[82:85], v[70:73]
	s_nop 2
	buffer_load_dwordx4 v[70:73], v7, s[4:7], 0 offen nt
	v_or_b32_e32 v7, 0x14000, v6
	buffer_load_dwordx4 v[78:81], v7, s[4:7], 0 offen nt
	v_or_b32_e32 v7, 0x16000, v6
	buffer_load_dwordx4 v[86:89], v7, s[4:7], 0 offen nt
	v_or_b32_e32 v7, 0x18000, v6
	buffer_load_dwordx4 v[94:97], v7, s[4:7], 0 offen nt
	v_or_b32_e32 v7, 0x1a000, v6
	buffer_load_dwordx4 v[146:149], v7, s[4:7], 0 offen nt
	v_or_b32_e32 v7, 0x1c000, v6
	v_or_b32_e32 v6, 0x1e000, v6
	buffer_load_dwordx4 v[150:153], v7, s[4:7], 0 offen nt
	buffer_load_dwordx4 v[154:157], v6, s[4:7], 0 offen nt
	v_add_u32_e32 v6, 8, v232
	v_and_b32_e32 v50, 56, v6
	v_lshl_or_b32 v6, v50, 10, v198
	ds_read_b128 v[6:9], v6
	v_lshl_or_b32 v18, v50, 8, v204
	ds_read_b128 v[18:21], v18
	ds_read_b128 v[26:29], v223
	v_or_b32_e32 v34, 1, v50
	s_movk_i32 s24, 0x1000
	s_waitcnt lgkmcnt(0)
	v_mfma_f32_16x16x32_bf16 v[18:21], v[18:21], v[26:29], v[74:77]
	v_add_u32_e32 v234, 5, v200
	v_mfma_f32_16x16x32_bf16 v[6:9], v[6:9], v[26:29], v[66:69]
	v_lshl_or_b32 v26, v34, 10, v198
	ds_read_b128 v[26:29], v26
	v_lshl_or_b32 v34, v34, 8, v204
	ds_read_b128 v[34:37], v34
	ds_read_b128 v[42:45], v222
	s_waitcnt lgkmcnt(0)
	v_mfma_f32_16x16x32_bf16 v[18:21], v[34:37], v[42:45], v[18:21]
	v_or_b32_e32 v34, 2, v50
	v_mfma_f32_16x16x32_bf16 v[6:9], v[26:29], v[42:45], v[6:9]
	v_lshl_or_b32 v26, v34, 10, v198
	ds_read_b128 v[26:29], v26
	v_lshl_or_b32 v34, v34, 8, v204
	ds_read_b128 v[34:37], v34
	ds_read_b128 v[42:45], v221
	s_waitcnt lgkmcnt(0)
	v_mfma_f32_16x16x32_bf16 v[18:21], v[34:37], v[42:45], v[18:21]
	v_or_b32_e32 v34, 3, v50
	v_mfma_f32_16x16x32_bf16 v[6:9], v[26:29], v[42:45], v[6:9]
	v_lshl_or_b32 v26, v34, 10, v198
	ds_read_b128 v[26:29], v26
	v_lshl_or_b32 v34, v34, 8, v204
	ds_read_b128 v[34:37], v34
	ds_read_b128 v[42:45], v219
	s_waitcnt lgkmcnt(0)
	v_mfma_f32_16x16x32_bf16 v[18:21], v[34:37], v[42:45], v[18:21]
	v_or_b32_e32 v34, 4, v50
	v_mfma_f32_16x16x32_bf16 v[6:9], v[26:29], v[42:45], v[6:9]
	v_lshl_or_b32 v26, v34, 10, v198
	ds_read_b128 v[26:29], v26
	v_lshl_or_b32 v34, v34, 8, v204
	ds_read_b128 v[34:37], v34
	ds_read_b128 v[42:45], v218
	s_waitcnt lgkmcnt(0)
	v_mfma_f32_16x16x32_bf16 v[18:21], v[34:37], v[42:45], v[18:21]
	v_or_b32_e32 v34, 5, v50
	v_mfma_f32_16x16x32_bf16 v[6:9], v[26:29], v[42:45], v[6:9]
	v_lshl_or_b32 v26, v34, 10, v198
	ds_read_b128 v[26:29], v26
	v_lshl_or_b32 v34, v34, 8, v204
	ds_read_b128 v[34:37], v34
	ds_read_b128 v[42:45], v217
	s_waitcnt lgkmcnt(0)
	v_mfma_f32_16x16x32_bf16 v[18:21], v[34:37], v[42:45], v[18:21]
	v_or_b32_e32 v34, 6, v50
	v_mfma_f32_16x16x32_bf16 v[6:9], v[26:29], v[42:45], v[6:9]
	v_lshl_or_b32 v26, v34, 10, v198
	ds_read_b128 v[26:29], v26
	v_lshl_or_b32 v34, v34, 8, v204
	ds_read_b128 v[34:37], v34
	ds_read_b128 v[42:45], v216
	s_waitcnt lgkmcnt(0)
	v_mfma_f32_16x16x32_bf16 v[18:21], v[34:37], v[42:45], v[18:21]
	v_or_b32_e32 v34, 7, v50
	v_mfma_f32_16x16x32_bf16 v[6:9], v[26:29], v[42:45], v[6:9]
	v_lshl_or_b32 v26, v34, 10, v198
	ds_read_b128 v[26:29], v26
	v_lshl_or_b32 v34, v34, 8, v204
	ds_read_b128 v[34:37], v34
	ds_read_b128 v[42:45], v213
	s_waitcnt lgkmcnt(0)
	v_mfma_f32_16x16x32_bf16 v[162:165], v[26:29], v[42:45], v[6:9]
	s_waitcnt vmcnt(31)
	s_nop 1
	v_cvt_pk_bf16_f32 v6, v102, v103
	v_cvt_pk_bf16_f32 v7, v104, v105
	ds_write_b64 v212, v[6:7]
	s_waitcnt vmcnt(30)
	v_cvt_pk_bf16_f32 v6, v98, v99
	v_cvt_pk_bf16_f32 v7, v100, v101
	ds_write_b64 v211, v[6:7] offset:512
	s_waitcnt vmcnt(29)
	v_cvt_pk_bf16_f32 v6, v110, v111
	v_cvt_pk_bf16_f32 v7, v112, v113
	ds_write_b64 v210, v[6:7] offset:1024
	s_waitcnt vmcnt(28)
	v_cvt_pk_bf16_f32 v6, v106, v107
	v_cvt_pk_bf16_f32 v7, v108, v109
	ds_write_b64 v209, v[6:7] offset:1536
	s_waitcnt vmcnt(27)
	v_cvt_pk_bf16_f32 v6, v118, v119
	v_cvt_pk_bf16_f32 v7, v120, v121
	ds_write_b64 v208, v[6:7] offset:2048
	s_waitcnt vmcnt(26)
	v_cvt_pk_bf16_f32 v6, v114, v115
	v_cvt_pk_bf16_f32 v7, v116, v117
	ds_write_b64 v207, v[6:7] offset:2560
	s_waitcnt vmcnt(25)
	v_cvt_pk_bf16_f32 v6, v126, v127
	v_cvt_pk_bf16_f32 v7, v128, v129
	ds_write_b64 v206, v[6:7] offset:3072
	s_waitcnt vmcnt(24)
	v_cvt_pk_bf16_f32 v6, v122, v123
	v_cvt_pk_bf16_f32 v7, v124, v125
	ds_write_b64 v205, v[6:7] offset:3584
	s_waitcnt vmcnt(23)
	v_cvt_pk_bf16_f32 v6, v134, v135
	v_cvt_pk_bf16_f32 v7, v136, v137
	ds_write_b64 v231, v[6:7] offset:4096
	s_waitcnt vmcnt(22)
	v_cvt_pk_bf16_f32 v6, v130, v131
	v_cvt_pk_bf16_f32 v7, v132, v133
	ds_write_b64 v230, v[6:7] offset:4608
	s_waitcnt vmcnt(21)
	v_cvt_pk_bf16_f32 v6, v142, v143
	v_cvt_pk_bf16_f32 v7, v144, v145
	ds_write_b64 v229, v[6:7] offset:5120
	s_waitcnt vmcnt(20)
	v_cvt_pk_bf16_f32 v6, v138, v139
	v_cvt_pk_bf16_f32 v7, v140, v141
	ds_write_b64 v228, v[6:7] offset:5632
	s_waitcnt vmcnt(19)
	v_cvt_pk_bf16_f32 v6, v170, v171
	v_cvt_pk_bf16_f32 v7, v172, v173
	ds_write_b64 v227, v[6:7] offset:6144
	s_waitcnt vmcnt(18)
	v_cvt_pk_bf16_f32 v6, v158, v159
	v_mov_b32_e32 v106, 0x1000
	v_cvt_pk_bf16_f32 v7, v160, v161
	ds_write_b64 v226, v[6:7] offset:6656
	s_waitcnt vmcnt(17)
	v_cvt_pk_bf16_f32 v6, v190, v191
	v_bitop3_b32 v107, v233, s19, v106 bitop3:0xde
	v_mfma_f32_16x16x32_bf16 v[166:169], v[34:37], v[42:45], v[18:21]
	v_cvt_pk_bf16_f32 v7, v192, v193
	ds_write_b64 v225, v[6:7] offset:7168
	s_waitcnt vmcnt(16)
	v_cvt_pk_bf16_f32 v6, v186, v187
	v_bitop3_b32 v26, v233, s17, v106 bitop3:0xde
	v_bitop3_b32 v34, v233, s11, v106 bitop3:0xde
	v_bitop3_b32 v18, v233, s16, v106 bitop3:0xde
	v_bitop3_b32 v42, v233, s13, v106 bitop3:0xde
	v_bitop3_b32 v50, v233, s10, v106 bitop3:0xde
	v_bitop3_b32 v58, v233, s12, v106 bitop3:0xde
	v_bitop3_b32 v66, v233, s1, v106 bitop3:0xde
	v_bitop3_b32 v74, v233, s18, v106 bitop3:0xde
	v_bitop3_b32 v82, v233, s23, v106 bitop3:0xde
	v_bitop3_b32 v90, v233, s22, v106 bitop3:0xde
	v_bitop3_b32 v98, v233, s21, v106 bitop3:0xde
	v_bitop3_b32 v102, v233, s20, v106 bitop3:0xde
	buffer_load_dwordx4 v[110:113], v107, s[4:7], 0 offen nt
	v_bitop3_b32 v107, v233, s15, v106 bitop3:0xde
	v_bitop3_b32 v106, v233, s14, v106 bitop3:0xde
	v_cvt_pk_bf16_f32 v7, v188, v189
	ds_write_b64 v224, v[6:7] offset:7680
	v_bitop3_b32 v6, v203, s24, v196 bitop3:0x36
	buffer_load_dwordx4 v[42:45], v42, s[4:7], 0 offen nt
	s_nop 0
	buffer_load_dwordx4 v[50:53], v50, s[4:7], 0 offen nt
	s_nop 0
	buffer_load_dwordx4 v[58:61], v58, s[4:7], 0 offen nt
	s_nop 0
	buffer_load_dwordx4 v[66:69], v66, s[4:7], 0 offen nt
	s_nop 0
	buffer_load_dwordx4 v[74:77], v74, s[4:7], 0 offen nt
	s_nop 0
	buffer_load_dwordx4 v[82:85], v82, s[4:7], 0 offen nt
	s_nop 0
	buffer_load_dwordx4 v[90:93], v90, s[4:7], 0 offen nt
	s_nop 0
	buffer_load_dwordx4 v[98:101], v98, s[4:7], 0 offen nt
	s_nop 0
	buffer_load_dwordx4 v[102:105], v102, s[4:7], 0 offen nt
	s_nop 0
	buffer_load_dwordx4 v[126:129], v106, s[4:7], 0 offen nt
	buffer_load_dwordx4 v[118:121], v107, s[4:7], 0 offen nt
	s_nop 0
	buffer_load_dwordx4 v[6:9], v6, s[4:7], 0 offen nt
	s_nop 0
	buffer_load_dwordx4 v[18:21], v18, s[4:7], 0 offen nt
	s_nop 0
	buffer_load_dwordx4 v[26:29], v26, s[4:7], 0 offen nt
	s_nop 0
	buffer_load_dwordx4 v[34:37], v34, s[4:7], 0 offen nt
	v_add_u32_e32 v106, 16, v232
	v_and_b32_e32 v138, 56, v106
	v_lshl_or_b32 v106, v138, 10, v198
	ds_read_b128 v[106:109], v106
	v_lshl_or_b32 v114, v138, 8, v204
	ds_read_b128 v[114:117], v114
	ds_read_b128 v[122:125], v223
	v_or_b32_e32 v130, 1, v138
	s_waitcnt vmcnt(31)
	v_cvt_pk_bf16_f32 v2, v2, v3
	s_waitcnt lgkmcnt(0)
	v_mfma_f32_16x16x32_bf16 v[114:117], v[114:117], v[122:125], v[166:169]
	v_cvt_pk_bf16_f32 v3, v4, v5
	v_mfma_f32_16x16x32_bf16 v[106:109], v[106:109], v[122:125], v[162:165]
	v_lshl_or_b32 v122, v130, 10, v198
	ds_read_b128 v[122:125], v122
	v_lshl_or_b32 v130, v130, 8, v204
	ds_read_b128 v[130:133], v130
	ds_read_b128 v[134:137], v222
	s_waitcnt lgkmcnt(0)
	v_mfma_f32_16x16x32_bf16 v[114:117], v[130:133], v[134:137], v[114:117]
	v_or_b32_e32 v130, 2, v138
	v_mfma_f32_16x16x32_bf16 v[106:109], v[122:125], v[134:137], v[106:109]
	v_lshl_or_b32 v122, v130, 10, v198
	ds_read_b128 v[122:125], v122
	v_lshl_or_b32 v130, v130, 8, v204
	ds_read_b128 v[130:133], v130
	ds_read_b128 v[134:137], v221
	s_waitcnt lgkmcnt(0)
	v_mfma_f32_16x16x32_bf16 v[114:117], v[130:133], v[134:137], v[114:117]
	v_or_b32_e32 v130, 3, v138
	v_mfma_f32_16x16x32_bf16 v[106:109], v[122:125], v[134:137], v[106:109]
	v_lshl_or_b32 v122, v130, 10, v198
	ds_read_b128 v[122:125], v122
	v_lshl_or_b32 v130, v130, 8, v204
	ds_read_b128 v[130:133], v130
	ds_read_b128 v[134:137], v219
	s_waitcnt lgkmcnt(0)
	v_mfma_f32_16x16x32_bf16 v[114:117], v[130:133], v[134:137], v[114:117]
	v_or_b32_e32 v130, 4, v138
	v_mfma_f32_16x16x32_bf16 v[106:109], v[122:125], v[134:137], v[106:109]
	v_lshl_or_b32 v122, v130, 10, v198
	ds_read_b128 v[122:125], v122
	v_lshl_or_b32 v130, v130, 8, v204
	ds_read_b128 v[130:133], v130
	ds_read_b128 v[134:137], v218
	s_waitcnt lgkmcnt(0)
	v_mfma_f32_16x16x32_bf16 v[114:117], v[130:133], v[134:137], v[114:117]
	v_or_b32_e32 v130, 5, v138
	v_mfma_f32_16x16x32_bf16 v[106:109], v[122:125], v[134:137], v[106:109]
	v_lshl_or_b32 v122, v130, 10, v198
	ds_read_b128 v[122:125], v122
	v_lshl_or_b32 v130, v130, 8, v204
	ds_read_b128 v[130:133], v130
	ds_read_b128 v[134:137], v217
	s_waitcnt lgkmcnt(0)
	v_mfma_f32_16x16x32_bf16 v[114:117], v[130:133], v[134:137], v[114:117]
	v_or_b32_e32 v130, 6, v138
	v_mfma_f32_16x16x32_bf16 v[106:109], v[122:125], v[134:137], v[106:109]
	v_lshl_or_b32 v122, v130, 10, v198
	ds_read_b128 v[122:125], v122
	v_lshl_or_b32 v130, v130, 8, v204
	ds_read_b128 v[130:133], v130
	ds_read_b128 v[134:137], v216
	s_waitcnt lgkmcnt(0)
	v_mfma_f32_16x16x32_bf16 v[114:117], v[130:133], v[134:137], v[114:117]
	v_or_b32_e32 v130, 7, v138
	v_mfma_f32_16x16x32_bf16 v[106:109], v[122:125], v[134:137], v[106:109]
	v_lshl_or_b32 v122, v130, 10, v198
	v_lshl_or_b32 v130, v130, 8, v204
	ds_read_b128 v[122:125], v122
	ds_read_b128 v[134:137], v130
	ds_read_b128 v[138:141], v213
	ds_write_b64 v212, v[2:3]
	s_waitcnt vmcnt(30)
	v_cvt_pk_bf16_f32 v2, v10, v11
	v_cvt_pk_bf16_f32 v3, v12, v13
	ds_write_b64 v211, v[2:3] offset:512
	s_waitcnt vmcnt(29)
	v_cvt_pk_bf16_f32 v2, v14, v15
	v_cvt_pk_bf16_f32 v3, v16, v17
	ds_write_b64 v210, v[2:3] offset:1024
	s_waitcnt vmcnt(28)
	v_cvt_pk_bf16_f32 v2, v22, v23
	v_cvt_pk_bf16_f32 v3, v24, v25
	ds_write_b64 v209, v[2:3] offset:1536
	s_waitcnt vmcnt(27)
	v_cvt_pk_bf16_f32 v2, v30, v31
	v_cvt_pk_bf16_f32 v3, v32, v33
	ds_write_b64 v208, v[2:3] offset:2048
	s_waitcnt vmcnt(26)
	v_cvt_pk_bf16_f32 v2, v38, v39
	v_cvt_pk_bf16_f32 v3, v40, v41
	ds_write_b64 v207, v[2:3] offset:2560
	s_waitcnt vmcnt(25)
	v_cvt_pk_bf16_f32 v2, v46, v47
	v_cvt_pk_bf16_f32 v3, v48, v49
	ds_write_b64 v206, v[2:3] offset:3072
	s_waitcnt vmcnt(24)
	v_cvt_pk_bf16_f32 v2, v54, v55
	v_cvt_pk_bf16_f32 v3, v56, v57
	ds_write_b64 v205, v[2:3] offset:3584
	s_waitcnt vmcnt(23)
	v_cvt_pk_bf16_f32 v2, v62, v63
	v_cvt_pk_bf16_f32 v3, v64, v65
	ds_write_b64 v231, v[2:3] offset:4096
	s_waitcnt vmcnt(22)
	v_cvt_pk_bf16_f32 v2, v70, v71
	v_cvt_pk_bf16_f32 v3, v72, v73
	ds_write_b64 v230, v[2:3] offset:4608
	s_waitcnt vmcnt(21)
	v_cvt_pk_bf16_f32 v2, v78, v79
	v_cvt_pk_bf16_f32 v3, v80, v81
	ds_write_b64 v229, v[2:3] offset:5120
	s_waitcnt vmcnt(20)
	v_cvt_pk_bf16_f32 v2, v86, v87
	v_cvt_pk_bf16_f32 v3, v88, v89
	ds_write_b64 v228, v[2:3] offset:5632
	s_waitcnt vmcnt(19)
	v_cvt_pk_bf16_f32 v2, v94, v95
	v_cvt_pk_bf16_f32 v3, v96, v97
	ds_write_b64 v227, v[2:3] offset:6144
	s_waitcnt vmcnt(18)
	v_cvt_pk_bf16_f32 v2, v146, v147
	v_cvt_pk_bf16_f32 v3, v148, v149
	ds_write_b64 v226, v[2:3] offset:6656
	s_waitcnt vmcnt(17)
	v_cvt_pk_bf16_f32 v2, v150, v151
	v_cvt_pk_bf16_f32 v3, v152, v153
	ds_write_b64 v225, v[2:3] offset:7168
	s_waitcnt vmcnt(16)
	v_cvt_pk_bf16_f32 v2, v154, v155
	v_cvt_pk_bf16_f32 v3, v156, v157
	ds_write_b64 v224, v[2:3] offset:7680
	v_lshlrev_b32_e32 v2, 10, v234
	s_waitcnt lgkmcnt(14)
	v_mfma_f32_16x16x32_bf16 v[130:133], v[122:125], v[138:141], v[106:109]
	v_and_or_b32 v122, v2, s0, v203
	buffer_load_dwordx4 v[2:5], v122, s[4:7], 0 offen nt
	v_or_b32_e32 v10, 0x2000, v122
	v_mfma_f32_16x16x32_bf16 v[134:137], v[134:137], v[138:141], v[114:117]
	v_or_b32_e32 v14, 0x4000, v122
	v_or_b32_e32 v22, 0x6000, v122
	v_or_b32_e32 v30, 0x8000, v122
	v_or_b32_e32 v38, 0xa000, v122
	v_or_b32_e32 v46, 0xc000, v122
	v_or_b32_e32 v54, 0xe000, v122
	v_or_b32_e32 v62, 0x10000, v122
	v_or_b32_e32 v70, 0x12000, v122
	v_or_b32_e32 v78, 0x14000, v122
	v_or_b32_e32 v86, 0x16000, v122
	v_or_b32_e32 v94, 0x18000, v122
	v_or_b32_e32 v106, 0x1a000, v122
	v_or_b32_e32 v114, 0x1c000, v122
	v_or_b32_e32 v122, 0x1e000, v122
	buffer_load_dwordx4 v[54:57], v54, s[4:7], 0 offen nt
	s_nop 0
	buffer_load_dwordx4 v[62:65], v62, s[4:7], 0 offen nt
	s_nop 0
	buffer_load_dwordx4 v[70:73], v70, s[4:7], 0 offen nt
	s_nop 0
	buffer_load_dwordx4 v[78:81], v78, s[4:7], 0 offen nt
	s_nop 0
	buffer_load_dwordx4 v[86:89], v86, s[4:7], 0 offen nt
	s_nop 0
	buffer_load_dwordx4 v[94:97], v94, s[4:7], 0 offen nt
	s_nop 0
	buffer_load_dwordx4 v[106:109], v106, s[4:7], 0 offen nt
	s_nop 0
	buffer_load_dwordx4 v[114:117], v114, s[4:7], 0 offen nt
	s_nop 0
	buffer_load_dwordx4 v[122:125], v122, s[4:7], 0 offen nt
	s_nop 0
	buffer_load_dwordx4 v[10:13], v10, s[4:7], 0 offen nt
	s_nop 0
	buffer_load_dwordx4 v[14:17], v14, s[4:7], 0 offen nt
	s_nop 0
	buffer_load_dwordx4 v[22:25], v22, s[4:7], 0 offen nt
	s_nop 0
	buffer_load_dwordx4 v[30:33], v30, s[4:7], 0 offen nt
	s_nop 0
	buffer_load_dwordx4 v[38:41], v38, s[4:7], 0 offen nt
	s_nop 0
	buffer_load_dwordx4 v[46:49], v46, s[4:7], 0 offen nt
	v_lshlrev_b32_e32 v138, 3, v235
	v_and_b32_e32 v150, 56, v138
	v_lshl_or_b32 v138, v150, 10, v198
	ds_read_b128 v[138:141], v138
	v_lshl_or_b32 v142, v150, 8, v204
	ds_read_b128 v[142:145], v142
	ds_read_b128 v[146:149], v223
	s_waitcnt vmcnt(19)
	v_cvt_pk_bf16_f32 v6, v6, v7
	v_cvt_pk_bf16_f32 v7, v8, v9
	s_waitcnt lgkmcnt(0)
	v_mfma_f32_16x16x32_bf16 v[134:137], v[142:145], v[146:149], v[134:137]
	v_or_b32_e32 v142, 1, v150
	v_mfma_f32_16x16x32_bf16 v[130:133], v[138:141], v[146:149], v[130:133]
	v_lshl_or_b32 v138, v142, 10, v198
	ds_read_b128 v[138:141], v138
	v_lshl_or_b32 v142, v142, 8, v204
	ds_read_b128 v[142:145], v142
	ds_read_b128 v[146:149], v222
	s_waitcnt lgkmcnt(0)
	v_mfma_f32_16x16x32_bf16 v[134:137], v[142:145], v[146:149], v[134:137]
	v_or_b32_e32 v142, 2, v150
	v_mfma_f32_16x16x32_bf16 v[130:133], v[138:141], v[146:149], v[130:133]
	v_lshl_or_b32 v138, v142, 10, v198
	ds_read_b128 v[138:141], v138
	v_lshl_or_b32 v142, v142, 8, v204
	ds_read_b128 v[142:145], v142
	ds_read_b128 v[146:149], v221
	s_waitcnt lgkmcnt(0)
	v_mfma_f32_16x16x32_bf16 v[134:137], v[142:145], v[146:149], v[134:137]
	v_or_b32_e32 v142, 3, v150
	v_mfma_f32_16x16x32_bf16 v[130:133], v[138:141], v[146:149], v[130:133]
	v_lshl_or_b32 v138, v142, 10, v198
	ds_read_b128 v[138:141], v138
	v_lshl_or_b32 v142, v142, 8, v204
	ds_read_b128 v[142:145], v142
	ds_read_b128 v[146:149], v219
	s_waitcnt lgkmcnt(0)
	v_mfma_f32_16x16x32_bf16 v[134:137], v[142:145], v[146:149], v[134:137]
	v_or_b32_e32 v142, 4, v150
	v_mfma_f32_16x16x32_bf16 v[130:133], v[138:141], v[146:149], v[130:133]
	v_lshl_or_b32 v138, v142, 10, v198
	ds_read_b128 v[138:141], v138
	v_lshl_or_b32 v142, v142, 8, v204
	ds_read_b128 v[142:145], v142
	ds_read_b128 v[146:149], v218
	s_waitcnt lgkmcnt(0)
	v_mfma_f32_16x16x32_bf16 v[134:137], v[142:145], v[146:149], v[134:137]
	v_or_b32_e32 v142, 5, v150
	v_mfma_f32_16x16x32_bf16 v[130:133], v[138:141], v[146:149], v[130:133]
	v_lshl_or_b32 v138, v142, 10, v198
	ds_read_b128 v[138:141], v138
	v_lshl_or_b32 v142, v142, 8, v204
	ds_read_b128 v[142:145], v142
	ds_read_b128 v[146:149], v217
	s_waitcnt lgkmcnt(0)
	v_mfma_f32_16x16x32_bf16 v[134:137], v[142:145], v[146:149], v[134:137]
	v_or_b32_e32 v142, 6, v150
	v_mfma_f32_16x16x32_bf16 v[130:133], v[138:141], v[146:149], v[130:133]
	v_lshl_or_b32 v138, v142, 10, v198
	ds_read_b128 v[138:141], v138
	v_lshl_or_b32 v142, v142, 8, v204
	ds_read_b128 v[142:145], v142
	ds_read_b128 v[146:149], v216
	s_waitcnt lgkmcnt(0)
	v_mfma_f32_16x16x32_bf16 v[134:137], v[142:145], v[146:149], v[134:137]
	v_or_b32_e32 v142, 7, v150
	v_mfma_f32_16x16x32_bf16 v[130:133], v[138:141], v[146:149], v[130:133]
	v_lshl_or_b32 v138, v142, 10, v198
	v_lshl_or_b32 v142, v142, 8, v204
	ds_read_b128 v[138:141], v138
	ds_read_b128 v[142:145], v142
	ds_read_b128 v[146:149], v213
	ds_write_b64 v212, v[6:7]
	s_waitcnt vmcnt(18)
	v_cvt_pk_bf16_f32 v6, v18, v19
	v_cvt_pk_bf16_f32 v7, v20, v21
	ds_write_b64 v211, v[6:7] offset:512
	s_waitcnt vmcnt(17)
	v_cvt_pk_bf16_f32 v6, v26, v27
	v_cvt_pk_bf16_f32 v7, v28, v29
	ds_write_b64 v210, v[6:7] offset:1024
	s_waitcnt vmcnt(16)
	v_cvt_pk_bf16_f32 v6, v34, v35
	v_cvt_pk_bf16_f32 v7, v36, v37
	ds_write_b64 v209, v[6:7] offset:1536
	v_cvt_pk_bf16_f32 v6, v42, v43
	v_cvt_pk_bf16_f32 v7, v44, v45
	ds_write_b64 v208, v[6:7] offset:2048
	v_cvt_pk_bf16_f32 v6, v50, v51
	v_cvt_pk_bf16_f32 v7, v52, v53
	ds_write_b64 v207, v[6:7] offset:2560
	v_cvt_pk_bf16_f32 v6, v58, v59
	v_cvt_pk_bf16_f32 v7, v60, v61
	ds_write_b64 v206, v[6:7] offset:3072
	v_cvt_pk_bf16_f32 v6, v66, v67
	v_cvt_pk_bf16_f32 v7, v68, v69
	ds_write_b64 v205, v[6:7] offset:3584
	v_cvt_pk_bf16_f32 v6, v74, v75
	v_cvt_pk_bf16_f32 v7, v76, v77
	ds_write_b64 v231, v[6:7] offset:4096
	v_cvt_pk_bf16_f32 v6, v82, v83
	v_cvt_pk_bf16_f32 v7, v84, v85
	ds_write_b64 v230, v[6:7] offset:4608
	v_cvt_pk_bf16_f32 v6, v90, v91
	v_cvt_pk_bf16_f32 v7, v92, v93
	ds_write_b64 v229, v[6:7] offset:5120
	v_cvt_pk_bf16_f32 v6, v98, v99
	v_cvt_pk_bf16_f32 v7, v100, v101
	ds_write_b64 v228, v[6:7] offset:5632
	v_cvt_pk_bf16_f32 v6, v102, v103
	v_cvt_pk_bf16_f32 v7, v104, v105
	ds_write_b64 v227, v[6:7] offset:6144
	v_cvt_pk_bf16_f32 v6, v110, v111
	v_cvt_pk_bf16_f32 v7, v112, v113
	ds_write_b64 v226, v[6:7] offset:6656
	v_cvt_pk_bf16_f32 v6, v118, v119
	v_cvt_pk_bf16_f32 v7, v120, v121
	ds_write_b64 v225, v[6:7] offset:7168
	v_cvt_pk_bf16_f32 v6, v126, v127
	v_cvt_pk_bf16_f32 v7, v128, v129
	ds_write_b64 v224, v[6:7] offset:7680
	v_add_u32_e32 v6, 0x1800, v196
	v_and_or_b32 v126, v6, s0, v203
	buffer_load_dwordx4 v[6:9], v126, s[4:7], 0 offen nt
	v_or_b32_e32 v18, 0x2000, v126
	v_or_b32_e32 v26, 0x4000, v126
	v_or_b32_e32 v34, 0x6000, v126
	v_or_b32_e32 v42, 0x8000, v126
	v_or_b32_e32 v50, 0xa000, v126
	v_or_b32_e32 v58, 0xc000, v126
	v_or_b32_e32 v66, 0xe000, v126
	v_or_b32_e32 v74, 0x10000, v126
	v_or_b32_e32 v82, 0x12000, v126
	v_or_b32_e32 v90, 0x14000, v126
	v_or_b32_e32 v98, 0x16000, v126
	v_or_b32_e32 v102, 0x18000, v126
	v_or_b32_e32 v110, 0x1a000, v126
	v_or_b32_e32 v118, 0x1c000, v126
	v_or_b32_e32 v126, 0x1e000, v126
	buffer_load_dwordx4 v[50:53], v50, s[4:7], 0 offen nt
	s_waitcnt lgkmcnt(14)
	v_mfma_f32_16x16x32_bf16 v[130:133], v[138:141], v[146:149], v[130:133]
	buffer_load_dwordx4 v[58:61], v58, s[4:7], 0 offen nt
	s_nop 0
	buffer_load_dwordx4 v[66:69], v66, s[4:7], 0 offen nt
	v_mfma_f32_16x16x32_bf16 v[134:137], v[142:145], v[146:149], v[134:137]
	buffer_load_dwordx4 v[74:77], v74, s[4:7], 0 offen nt
	v_add_u32_e32 v142, 7, v200
	buffer_load_dwordx4 v[82:85], v82, s[4:7], 0 offen nt
	s_nop 0
	buffer_load_dwordx4 v[90:93], v90, s[4:7], 0 offen nt
	s_nop 0
	buffer_load_dwordx4 v[98:101], v98, s[4:7], 0 offen nt
	s_nop 0
	buffer_load_dwordx4 v[102:105], v102, s[4:7], 0 offen nt
	s_nop 0
	buffer_load_dwordx4 v[110:113], v110, s[4:7], 0 offen nt
	s_nop 0
	buffer_load_dwordx4 v[118:121], v118, s[4:7], 0 offen nt
	s_nop 0
	buffer_load_dwordx4 v[126:129], v126, s[4:7], 0 offen nt
	s_nop 0
	buffer_load_dwordx4 v[18:21], v18, s[4:7], 0 offen nt
	s_nop 0
	buffer_load_dwordx4 v[26:29], v26, s[4:7], 0 offen nt
	s_nop 0
	buffer_load_dwordx4 v[34:37], v34, s[4:7], 0 offen nt
	s_nop 0
	buffer_load_dwordx4 v[42:45], v42, s[4:7], 0 offen nt
	v_xor_b32_e32 v143, 32, v232
	v_lshl_or_b32 v138, v143, 10, v198
	ds_read_b128 v[138:141], v138
	v_lshl_or_b32 v143, v143, 8, v204
	ds_read_b128 v[144:147], v143
	ds_read_b128 v[148:151], v223
	v_bitop3_b32 v143, v232, 1, 32 bitop3:0xde
	s_waitcnt vmcnt(31)
	v_cvt_pk_bf16_f32 v2, v2, v3
	s_waitcnt lgkmcnt(0)
	v_mfma_f32_16x16x32_bf16 v[134:137], v[144:147], v[148:151], v[134:137]
	v_cvt_pk_bf16_f32 v3, v4, v5
	v_mfma_f32_16x16x32_bf16 v[130:133], v[138:141], v[148:151], v[130:133]
	v_lshl_or_b32 v138, v143, 10, v198
	ds_read_b128 v[138:141], v138
	v_lshl_or_b32 v143, v143, 8, v204
	ds_read_b128 v[144:147], v143
	ds_read_b128 v[148:151], v222
	v_bitop3_b32 v143, v232, 2, 32 bitop3:0xde
	s_waitcnt lgkmcnt(0)
	v_mfma_f32_16x16x32_bf16 v[134:137], v[144:147], v[148:151], v[134:137]
	v_mfma_f32_16x16x32_bf16 v[130:133], v[138:141], v[148:151], v[130:133]
	v_lshl_or_b32 v138, v143, 10, v198
	ds_read_b128 v[138:141], v138
	v_lshl_or_b32 v143, v143, 8, v204
	ds_read_b128 v[144:147], v143
	ds_read_b128 v[148:151], v221
	v_bitop3_b32 v143, v232, 3, 32 bitop3:0xde
	s_waitcnt lgkmcnt(0)
	v_mfma_f32_16x16x32_bf16 v[130:133], v[138:141], v[148:151], v[130:133]
	v_lshl_or_b32 v138, v143, 10, v198
	ds_read_b128 v[138:141], v138
	v_lshl_or_b32 v143, v143, 8, v204
	v_mfma_f32_16x16x32_bf16 v[134:137], v[144:147], v[148:151], v[134:137]
	ds_read_b128 v[144:147], v143
	ds_read_b128 v[148:151], v219
	v_bitop3_b32 v143, v232, 4, 32 bitop3:0xde
	s_waitcnt lgkmcnt(0)
	v_mfma_f32_16x16x32_bf16 v[130:133], v[138:141], v[148:151], v[130:133]
	v_lshl_or_b32 v138, v143, 10, v198
	ds_read_b128 v[138:141], v138
	v_lshl_or_b32 v143, v143, 8, v204
	v_mfma_f32_16x16x32_bf16 v[134:137], v[144:147], v[148:151], v[134:137]
	ds_read_b128 v[144:147], v143
	ds_read_b128 v[148:151], v218
	v_bitop3_b32 v143, v232, 5, 32 bitop3:0xde
	s_waitcnt lgkmcnt(0)
	v_mfma_f32_16x16x32_bf16 v[130:133], v[138:141], v[148:151], v[130:133]
	v_lshl_or_b32 v138, v143, 10, v198
	ds_read_b128 v[138:141], v138
	v_lshl_or_b32 v143, v143, 8, v204
	v_mfma_f32_16x16x32_bf16 v[134:137], v[144:147], v[148:151], v[134:137]
	ds_read_b128 v[144:147], v143
	ds_read_b128 v[148:151], v217
	v_bitop3_b32 v143, v232, 6, 32 bitop3:0xde
	s_waitcnt lgkmcnt(0)
	v_mfma_f32_16x16x32_bf16 v[130:133], v[138:141], v[148:151], v[130:133]
	v_lshl_or_b32 v138, v143, 10, v198
	ds_read_b128 v[138:141], v138
	v_lshl_or_b32 v143, v143, 8, v204
	v_mfma_f32_16x16x32_bf16 v[134:137], v[144:147], v[148:151], v[134:137]
	ds_read_b128 v[144:147], v143
	ds_read_b128 v[148:151], v216
	v_bitop3_b32 v143, v232, 7, 32 bitop3:0xde
	s_waitcnt lgkmcnt(0)
	v_mfma_f32_16x16x32_bf16 v[130:133], v[138:141], v[148:151], v[130:133]
	v_lshl_or_b32 v138, v143, 10, v198
	v_lshl_or_b32 v143, v143, 8, v204
	ds_read_b128 v[138:141], v138
	v_mfma_f32_16x16x32_bf16 v[134:137], v[144:147], v[148:151], v[134:137]
	ds_read_b128 v[144:147], v143
	ds_read_b128 v[148:151], v213
	ds_write_b64 v212, v[2:3]
	s_waitcnt vmcnt(21)
	v_cvt_pk_bf16_f32 v2, v10, v11
	v_cvt_pk_bf16_f32 v3, v12, v13
	ds_write_b64 v211, v[2:3] offset:512
	s_waitcnt vmcnt(20)
	v_cvt_pk_bf16_f32 v2, v14, v15
	v_cvt_pk_bf16_f32 v3, v16, v17
	ds_write_b64 v210, v[2:3] offset:1024
	s_waitcnt vmcnt(19)
	v_cvt_pk_bf16_f32 v2, v22, v23
	v_cvt_pk_bf16_f32 v3, v24, v25
	ds_write_b64 v209, v[2:3] offset:1536
	s_waitcnt vmcnt(18)
	v_cvt_pk_bf16_f32 v2, v30, v31
	v_cvt_pk_bf16_f32 v3, v32, v33
	ds_write_b64 v208, v[2:3] offset:2048
	s_waitcnt vmcnt(17)
	v_cvt_pk_bf16_f32 v2, v38, v39
	v_cvt_pk_bf16_f32 v3, v40, v41
	ds_write_b64 v207, v[2:3] offset:2560
	s_waitcnt vmcnt(16)
	v_cvt_pk_bf16_f32 v2, v46, v47
	v_cvt_pk_bf16_f32 v3, v48, v49
	ds_write_b64 v206, v[2:3] offset:3072
	v_cvt_pk_bf16_f32 v2, v54, v55
	v_cvt_pk_bf16_f32 v3, v56, v57
	ds_write_b64 v205, v[2:3] offset:3584
	v_cvt_pk_bf16_f32 v2, v62, v63
	v_cvt_pk_bf16_f32 v3, v64, v65
	ds_write_b64 v231, v[2:3] offset:4096
	v_cvt_pk_bf16_f32 v2, v70, v71
	v_cvt_pk_bf16_f32 v3, v72, v73
	ds_write_b64 v230, v[2:3] offset:4608
	v_cvt_pk_bf16_f32 v2, v78, v79
	v_cvt_pk_bf16_f32 v3, v80, v81
	ds_write_b64 v229, v[2:3] offset:5120
	v_cvt_pk_bf16_f32 v2, v86, v87
	v_cvt_pk_bf16_f32 v3, v88, v89
	ds_write_b64 v228, v[2:3] offset:5632
	v_cvt_pk_bf16_f32 v2, v94, v95
	v_cvt_pk_bf16_f32 v3, v96, v97
	ds_write_b64 v227, v[2:3] offset:6144
	v_cvt_pk_bf16_f32 v2, v106, v107
	v_cvt_pk_bf16_f32 v3, v108, v109
	ds_write_b64 v226, v[2:3] offset:6656
	v_cvt_pk_bf16_f32 v2, v114, v115
	v_cvt_pk_bf16_f32 v3, v116, v117
	ds_write_b64 v225, v[2:3] offset:7168
	v_cvt_pk_bf16_f32 v2, v122, v123
	v_cvt_pk_bf16_f32 v3, v124, v125
	ds_write_b64 v224, v[2:3] offset:7680
	v_lshlrev_b32_e32 v2, 10, v142
	v_and_or_b32 v2, v2, s0, v203
	v_or_b32_e32 v3, 0x2000, v2
	buffer_load_dwordx4 v[10:13], v2, s[4:7], 0 offen nt
	buffer_load_dwordx4 v[14:17], v3, s[4:7], 0 offen nt
	v_or_b32_e32 v3, 0x4000, v2
	buffer_load_dwordx4 v[22:25], v3, s[4:7], 0 offen nt
	v_or_b32_e32 v3, 0x6000, v2
	buffer_load_dwordx4 v[30:33], v3, s[4:7], 0 offen nt
	v_or_b32_e32 v3, 0x8000, v2
	buffer_load_dwordx4 v[38:41], v3, s[4:7], 0 offen nt
	v_or_b32_e32 v3, 0xa000, v2
	buffer_load_dwordx4 v[46:49], v3, s[4:7], 0 offen nt
	v_or_b32_e32 v3, 0xc000, v2
	buffer_load_dwordx4 v[54:57], v3, s[4:7], 0 offen nt
	v_or_b32_e32 v3, 0xe000, v2
	buffer_load_dwordx4 v[62:65], v3, s[4:7], 0 offen nt
	v_or_b32_e32 v3, 0x10000, v2
	buffer_load_dwordx4 v[70:73], v3, s[4:7], 0 offen nt
	v_or_b32_e32 v3, 0x12000, v2
	buffer_load_dwordx4 v[78:81], v3, s[4:7], 0 offen nt
	v_or_b32_e32 v3, 0x14000, v2
	buffer_load_dwordx4 v[86:89], v3, s[4:7], 0 offen nt
	v_or_b32_e32 v3, 0x16000, v2
	buffer_load_dwordx4 v[94:97], v3, s[4:7], 0 offen nt
	v_or_b32_e32 v3, 0x18000, v2
	buffer_load_dwordx4 v[106:109], v3, s[4:7], 0 offen nt
	v_or_b32_e32 v3, 0x1a000, v2
	buffer_load_dwordx4 v[114:117], v3, s[4:7], 0 offen nt
	v_or_b32_e32 v3, 0x1c000, v2
	v_or_b32_e32 v2, 0x1e000, v2
	s_waitcnt lgkmcnt(14)
	v_mfma_f32_16x16x32_bf16 v[138:141], v[138:141], v[148:151], v[130:133]
	buffer_load_dwordx4 v[122:125], v3, s[4:7], 0 offen nt
	s_nop 1
	buffer_load_dwordx4 v[130:133], v2, s[4:7], 0 offen nt
	v_mfma_f32_16x16x32_bf16 v[134:137], v[144:147], v[148:151], v[134:137]
	v_lshlrev_b32_e32 v2, 3, v234
	v_and_b32_e32 v143, 56, v2
	v_lshl_or_b32 v2, v143, 10, v198
	v_lshl_or_b32 v152, v143, 8, v204
	ds_read_b128 v[2:5], v2
	ds_read_b128 v[144:147], v223
	ds_read_b128 v[148:151], v222
	ds_read_b128 v[152:155], v152
	v_or_b32_e32 v156, 1, v143
	v_lshl_or_b32 v157, v156, 10, v198
	s_waitcnt lgkmcnt(2)
	v_mfma_f32_16x16x32_bf16 v[2:5], v[2:5], v[144:147], v[138:141]
	s_waitcnt vmcnt(31)
	v_cvt_pk_bf16_f32 v6, v6, v7
	v_cvt_pk_bf16_f32 v7, v8, v9
	s_waitcnt lgkmcnt(0)
	v_mfma_f32_16x16x32_bf16 v[134:137], v[152:155], v[144:147], v[134:137]
	ds_read_b128 v[138:141], v157
	v_lshl_or_b32 v144, v156, 8, v204
	ds_read_b128 v[144:147], v144
	v_or_b32_e32 v156, 2, v143
	s_waitcnt lgkmcnt(1)
	v_mfma_f32_16x16x32_bf16 v[2:5], v[138:141], v[148:151], v[2:5]
	v_lshl_or_b32 v138, v156, 10, v198
	ds_read_b128 v[138:141], v138
	ds_read_b128 v[152:155], v221
	s_waitcnt lgkmcnt(2)
	v_mfma_f32_16x16x32_bf16 v[134:137], v[144:147], v[148:151], v[134:137]
	v_lshl_or_b32 v144, v156, 8, v204
	v_or_b32_e32 v156, 3, v143
	ds_read_b128 v[144:147], v144
	ds_read_b128 v[148:151], v219
	s_waitcnt lgkmcnt(2)
	v_mfma_f32_16x16x32_bf16 v[2:5], v[138:141], v[152:155], v[2:5]
	v_lshl_or_b32 v138, v156, 10, v198
	ds_read_b128 v[138:141], v138
	s_waitcnt lgkmcnt(2)
	v_mfma_f32_16x16x32_bf16 v[134:137], v[144:147], v[152:155], v[134:137]
	v_lshl_or_b32 v144, v156, 8, v204
	ds_read_b128 v[144:147], v144
	v_or_b32_e32 v152, 4, v143
	s_waitcnt lgkmcnt(1)
	v_mfma_f32_16x16x32_bf16 v[2:5], v[138:141], v[148:151], v[2:5]
	v_lshl_or_b32 v138, v152, 10, v198
	ds_read_b128 v[138:141], v138
	v_or_b32_e32 v156, 5, v143
	s_waitcnt lgkmcnt(1)
	v_mfma_f32_16x16x32_bf16 v[134:137], v[144:147], v[148:151], v[134:137]
	ds_read_b128 v[144:147], v218
	v_lshl_or_b32 v148, v152, 8, v204
	ds_read_b128 v[148:151], v148
	ds_read_b128 v[152:155], v217
	s_waitcnt lgkmcnt(2)
	v_mfma_f32_16x16x32_bf16 v[2:5], v[138:141], v[144:147], v[2:5]
	v_lshl_or_b32 v138, v156, 10, v198
	ds_read_b128 v[138:141], v138
	s_waitcnt lgkmcnt(2)
	v_mfma_f32_16x16x32_bf16 v[134:137], v[148:151], v[144:147], v[134:137]
	v_lshl_or_b32 v144, v156, 8, v204
	ds_read_b128 v[144:147], v144
	v_or_b32_e32 v148, 6, v143
	s_waitcnt lgkmcnt(1)
	v_mfma_f32_16x16x32_bf16 v[2:5], v[138:141], v[152:155], v[2:5]
	v_lshl_or_b32 v138, v148, 10, v198
	ds_read_b128 v[138:141], v138
	v_lshl_or_b32 v148, v148, 8, v204
	s_waitcnt lgkmcnt(1)
	v_mfma_f32_16x16x32_bf16 v[134:137], v[144:147], v[152:155], v[134:137]
	ds_read_b128 v[144:147], v216
	ds_read_b128 v[148:151], v148
	ds_read_b128 v[152:155], v213
	v_or_b32_e32 v143, 7, v143
	ds_write_b64 v212, v[6:7]
	s_waitcnt lgkmcnt(3)
	v_mfma_f32_16x16x32_bf16 v[2:5], v[138:141], v[144:147], v[2:5]
	v_lshl_or_b32 v138, v143, 10, v198
	v_lshl_or_b32 v143, v143, 8, v204
	s_waitcnt vmcnt(19)
	v_cvt_pk_bf16_f32 v6, v18, v19
	v_cvt_pk_bf16_f32 v7, v20, v21
	ds_read_b128 v[138:141], v138
	s_waitcnt lgkmcnt(3)
	v_mfma_f32_16x16x32_bf16 v[134:137], v[148:151], v[144:147], v[134:137]
	ds_read_b128 v[144:147], v143
	ds_write_b64 v211, v[6:7] offset:512
	s_waitcnt vmcnt(18)
	v_cvt_pk_bf16_f32 v6, v26, v27
	v_cvt_pk_bf16_f32 v7, v28, v29
	ds_write_b64 v210, v[6:7] offset:1024
	s_waitcnt vmcnt(17)
	v_cvt_pk_bf16_f32 v6, v34, v35
	v_cvt_pk_bf16_f32 v7, v36, v37
	ds_write_b64 v209, v[6:7] offset:1536
	s_waitcnt vmcnt(16)
	v_cvt_pk_bf16_f32 v6, v42, v43
	v_cvt_pk_bf16_f32 v7, v44, v45
	ds_write_b64 v208, v[6:7] offset:2048
	v_cvt_pk_bf16_f32 v6, v50, v51
	v_cvt_pk_bf16_f32 v7, v52, v53
	ds_write_b64 v207, v[6:7] offset:2560
	v_cvt_pk_bf16_f32 v6, v58, v59
	v_cvt_pk_bf16_f32 v7, v60, v61
	ds_write_b64 v206, v[6:7] offset:3072
	v_cvt_pk_bf16_f32 v6, v66, v67
	v_cvt_pk_bf16_f32 v7, v68, v69
	ds_write_b64 v205, v[6:7] offset:3584
	v_cvt_pk_bf16_f32 v6, v74, v75
	v_cvt_pk_bf16_f32 v7, v76, v77
	ds_write_b64 v231, v[6:7] offset:4096
	v_cvt_pk_bf16_f32 v6, v82, v83
	v_cvt_pk_bf16_f32 v7, v84, v85
	ds_write_b64 v230, v[6:7] offset:4608
	v_cvt_pk_bf16_f32 v6, v90, v91
	v_cvt_pk_bf16_f32 v7, v92, v93
	s_waitcnt lgkmcnt(9)
	v_mfma_f32_16x16x32_bf16 v[134:137], v[144:147], v[152:155], v[134:137]
	ds_write_b64 v229, v[6:7] offset:5120
	v_cvt_pk_bf16_f32 v6, v98, v99
	v_cvt_pk_bf16_f32 v7, v100, v101
	ds_write_b64 v228, v[6:7] offset:5632
	v_cvt_pk_bf16_f32 v6, v102, v103
	v_cvt_pk_bf16_f32 v7, v104, v105
	ds_write_b64 v227, v[6:7] offset:6144
	v_cvt_pk_bf16_f32 v6, v110, v111
	v_cvt_pk_bf16_f32 v7, v112, v113
	ds_write_b64 v226, v[6:7] offset:6656
	v_cvt_pk_bf16_f32 v6, v118, v119
	v_cvt_pk_bf16_f32 v7, v120, v121
	v_mfma_f32_16x16x32_bf16 v[2:5], v[138:141], v[152:155], v[2:5]
	ds_write_b64 v225, v[6:7] offset:7168
	v_cvt_pk_bf16_f32 v6, v126, v127
	v_cvt_pk_bf16_f32 v7, v128, v129
	ds_write_b64 v224, v[6:7] offset:7680
	v_add_u32_e32 v6, 48, v232
	v_and_b32_e32 v50, 56, v6
	v_lshl_or_b32 v6, v50, 10, v198
	v_lshl_or_b32 v34, v50, 8, v204
	ds_read_b128 v[6:9], v6
	ds_read_b128 v[18:21], v223
	ds_read_b128 v[26:29], v222
	ds_read_b128 v[34:37], v34
	v_or_b32_e32 v42, 1, v50
	v_lshl_or_b32 v43, v42, 10, v198
	s_waitcnt lgkmcnt(2)
	v_mfma_f32_16x16x32_bf16 v[2:5], v[6:9], v[18:21], v[2:5]
	ds_read_b128 v[6:9], v43
	v_or_b32_e32 v51, 2, v50
	s_waitcnt lgkmcnt(1)
	v_mfma_f32_16x16x32_bf16 v[18:21], v[34:37], v[18:21], v[134:137]
	v_lshl_or_b32 v34, v42, 8, v204
	ds_read_b128 v[34:37], v34
	s_waitcnt lgkmcnt(1)
	v_mfma_f32_16x16x32_bf16 v[2:5], v[6:9], v[26:29], v[2:5]
	v_lshl_or_b32 v6, v51, 10, v198
	ds_read_b128 v[6:9], v6
	ds_read_b128 v[42:45], v221
	s_waitcnt lgkmcnt(2)
	v_mfma_f32_16x16x32_bf16 v[18:21], v[34:37], v[26:29], v[18:21]
	v_lshl_or_b32 v26, v51, 8, v204
	v_or_b32_e32 v51, 3, v50
	ds_read_b128 v[26:29], v26
	ds_read_b128 v[34:37], v219
	s_waitcnt lgkmcnt(2)
	v_mfma_f32_16x16x32_bf16 v[2:5], v[6:9], v[42:45], v[2:5]
	v_lshl_or_b32 v6, v51, 10, v198
	ds_read_b128 v[6:9], v6
	s_waitcnt lgkmcnt(2)
	v_mfma_f32_16x16x32_bf16 v[18:21], v[26:29], v[42:45], v[18:21]
	v_lshl_or_b32 v26, v51, 8, v204
	ds_read_b128 v[26:29], v26
	v_or_b32_e32 v42, 4, v50
	s_waitcnt lgkmcnt(1)
	v_mfma_f32_16x16x32_bf16 v[2:5], v[6:9], v[34:37], v[2:5]
	v_lshl_or_b32 v6, v42, 10, v198
	ds_read_b128 v[6:9], v6
	v_or_b32_e32 v51, 5, v50
	s_waitcnt lgkmcnt(1)
	v_mfma_f32_16x16x32_bf16 v[18:21], v[26:29], v[34:37], v[18:21]
	ds_read_b128 v[26:29], v218
	v_lshl_or_b32 v34, v42, 8, v204
	ds_read_b128 v[34:37], v34
	ds_read_b128 v[42:45], v217
	s_waitcnt lgkmcnt(2)
	v_mfma_f32_16x16x32_bf16 v[2:5], v[6:9], v[26:29], v[2:5]
	v_lshl_or_b32 v6, v51, 10, v198
	ds_read_b128 v[6:9], v6
	s_waitcnt lgkmcnt(2)
	v_mfma_f32_16x16x32_bf16 v[18:21], v[34:37], v[26:29], v[18:21]
	v_lshl_or_b32 v26, v51, 8, v204
	ds_read_b128 v[26:29], v26
	v_or_b32_e32 v34, 6, v50
	s_waitcnt lgkmcnt(1)
	v_mfma_f32_16x16x32_bf16 v[2:5], v[6:9], v[42:45], v[2:5]
	v_lshl_or_b32 v6, v34, 10, v198
	ds_read_b128 v[6:9], v6
	v_lshl_or_b32 v34, v34, 8, v204
	s_waitcnt lgkmcnt(1)
	v_mfma_f32_16x16x32_bf16 v[18:21], v[26:29], v[42:45], v[18:21]
	ds_read_b128 v[26:29], v216
	ds_read_b128 v[34:37], v34
	ds_read_b128 v[42:45], v213
	v_or_b32_e32 v50, 7, v50
	s_waitcnt lgkmcnt(2)
	v_mfma_f32_16x16x32_bf16 v[2:5], v[6:9], v[26:29], v[2:5]
	v_lshl_or_b32 v6, v50, 10, v198
	ds_read_b128 v[6:9], v6
	s_waitcnt lgkmcnt(2)
	v_mfma_f32_16x16x32_bf16 v[18:21], v[34:37], v[26:29], v[18:21]
	v_lshl_or_b32 v26, v50, 8, v204
	ds_read_b128 v[26:29], v26
	s_waitcnt lgkmcnt(1)
	v_mfma_f32_16x16x32_bf16 v[34:37], v[6:9], v[42:45], v[2:5]
	v_and_b32_e32 v74, 7, v197
	v_lshrrev_b32_e32 v75, 3, v197
	v_lshlrev_b32_e32 v192, 13, v200
	v_lshlrev_b32_e32 v193, 11, v200
	v_lshl_add_u32 v203, v197, 2, v196
	v_lshl_or_b32 v192, v75, 8, v192
	v_lshl_or_b32 v193, v75, 6, v193
	v_add_u32_e32 v203, 0x24800, v203
	v_lshl_or_b32 v192, v201, 6, v192
	v_lshl_or_b32 v193, v74, 1, v193
	v_lshl_or_b32 v192, v74, 1, v192
	v_or_b32_e32 v193, 0x10000, v193
	v_cmp_gt_u32_e64 s[36:37], 16, v1
	v_cmp_eq_u32_e64 s[38:39], 1, v201
	ds_read2_b32 v[2:3], v203 offset1:16
	ds_read2_b32 v[4:5], v203 offset0:32 offset1:48
	ds_read2_b32 v[6:7], v203 offset0:64 offset1:80
	ds_read2_b32 v[8:9], v203 offset0:96 offset1:112
	ds_read2_b32 v[50:51], v203 offset0:128 offset1:144
	ds_read2_b32 v[52:53], v203 offset0:160 offset1:176
	ds_read2_b32 v[58:59], v203 offset0:192 offset1:208
	ds_read2_b32 v[60:61], v203 offset0:224 offset1:240
	v_mov_b32_e32 v146, 0
	v_mov_b32_e32 v147, 0
	v_mov_b32_e32 v150, 0
	v_mov_b32_e32 v151, 0
	v_mov_b32_e32 v154, 0
	v_mov_b32_e32 v155, 0
	v_mov_b32_e32 v158, 0
	v_mov_b32_e32 v159, 0
	v_mov_b32_e32 v162, 0
	v_mov_b32_e32 v163, 0
	v_mov_b32_e32 v166, 0
	v_mov_b32_e32 v167, 0
	v_mov_b32_e32 v170, 0
	v_mov_b32_e32 v171, 0
	v_mov_b32_e32 v174, 0
	v_mov_b32_e32 v175, 0
	v_mov_b32_e32 v178, 0
	v_mov_b32_e32 v179, 0
	v_mov_b32_e32 v182, 0
	v_mov_b32_e32 v183, 0
	v_mov_b32_e32 v186, 0
	v_mov_b32_e32 v187, 0
	v_mov_b32_e32 v190, 0
	v_mov_b32_e32 v191, 0
	v_mov_b32_e32 v234, 0
	v_mov_b32_e32 v235, 0
	v_mov_b32_e32 v238, 0
	v_mov_b32_e32 v239, 0
	v_mov_b32_e32 v242, 0
	v_mov_b32_e32 v243, 0
	v_mov_b32_e32 v246, 0
	v_mov_b32_e32 v247, 0
	ds_read_u16 v82, v192
	ds_read_u16 v83, v192 offset:16
	ds_read_u16 v84, v192 offset:32
	ds_read_u16 v85, v192 offset:48
	ds_read_u16 v90, v193
	ds_read_u16 v91, v193 offset:16
	ds_read_u16 v92, v193 offset:32
	ds_read_u16 v93, v193 offset:48
	ds_read_u16 v98, v192 offset:512
	ds_read_u16 v99, v192 offset:528
	ds_read_u16 v100, v192 offset:544
	ds_read_u16 v101, v192 offset:560
	ds_read_u16 v102, v193 offset:128
	ds_read_u16 v103, v193 offset:144
	ds_read_u16 v104, v193 offset:160
	ds_read_u16 v105, v193 offset:176
	s_waitcnt lgkmcnt(8)
	v_lshl_or_b32 v144, v83, 16, v82
	v_lshl_or_b32 v145, v85, 16, v84
	s_mov_b64 exec, s[36:37]
	v_lshl_or_b32 v146, v91, 16, v90
	v_lshl_or_b32 v147, v93, 16, v92
	s_mov_b64 exec, -1
	ds_read_u16 v82, v192 offset:1024
	ds_read_u16 v83, v192 offset:1040
	ds_read_u16 v84, v192 offset:1056
	ds_read_u16 v85, v192 offset:1072
	ds_read_u16 v90, v193 offset:256
	ds_read_u16 v91, v193 offset:272
	ds_read_u16 v92, v193 offset:288
	ds_read_u16 v93, v193 offset:304
	s_waitcnt lgkmcnt(8)
	v_lshl_or_b32 v148, v99, 16, v98
	v_lshl_or_b32 v149, v101, 16, v100
	s_mov_b64 exec, s[36:37]
	v_lshl_or_b32 v150, v103, 16, v102
	v_lshl_or_b32 v151, v105, 16, v104
	s_mov_b64 exec, -1
	ds_read_u16 v98, v192 offset:1536
	ds_read_u16 v99, v192 offset:1552
	ds_read_u16 v100, v192 offset:1568
	ds_read_u16 v101, v192 offset:1584
	ds_read_u16 v102, v193 offset:384
	ds_read_u16 v103, v193 offset:400
	ds_read_u16 v104, v193 offset:416
	ds_read_u16 v105, v193 offset:432
	s_waitcnt lgkmcnt(8)
	v_lshl_or_b32 v152, v83, 16, v82
	v_lshl_or_b32 v153, v85, 16, v84
	s_mov_b64 exec, s[36:37]
	v_lshl_or_b32 v154, v91, 16, v90
	v_lshl_or_b32 v155, v93, 16, v92
	s_mov_b64 exec, -1
	ds_read_u16 v82, v192 offset:2048
	ds_read_u16 v83, v192 offset:2064
	ds_read_u16 v84, v192 offset:2080
	ds_read_u16 v85, v192 offset:2096
	ds_read_u16 v90, v193 offset:512
	ds_read_u16 v91, v193 offset:528
	ds_read_u16 v92, v193 offset:544
	ds_read_u16 v93, v193 offset:560
	s_waitcnt lgkmcnt(8)
	v_lshl_or_b32 v156, v99, 16, v98
	v_lshl_or_b32 v157, v101, 16, v100
	s_mov_b64 exec, s[36:37]
	v_lshl_or_b32 v158, v103, 16, v102
	v_lshl_or_b32 v159, v105, 16, v104
	s_mov_b64 exec, -1
	ds_read_u16 v98, v192 offset:2560
	ds_read_u16 v99, v192 offset:2576
	ds_read_u16 v100, v192 offset:2592
	ds_read_u16 v101, v192 offset:2608
	ds_read_u16 v102, v193 offset:640
	ds_read_u16 v103, v193 offset:656
	ds_read_u16 v104, v193 offset:672
	ds_read_u16 v105, v193 offset:688
	s_waitcnt lgkmcnt(8)
	v_lshl_or_b32 v160, v83, 16, v82
	v_lshl_or_b32 v161, v85, 16, v84
	s_mov_b64 exec, s[36:37]
	v_lshl_or_b32 v162, v91, 16, v90
	v_lshl_or_b32 v163, v93, 16, v92
	s_mov_b64 exec, -1
	ds_read_u16 v82, v192 offset:3072
	ds_read_u16 v83, v192 offset:3088
	ds_read_u16 v84, v192 offset:3104
	ds_read_u16 v85, v192 offset:3120
	ds_read_u16 v90, v193 offset:768
	ds_read_u16 v91, v193 offset:784
	ds_read_u16 v92, v193 offset:800
	ds_read_u16 v93, v193 offset:816
	s_waitcnt lgkmcnt(8)
	v_lshl_or_b32 v164, v99, 16, v98
	v_lshl_or_b32 v165, v101, 16, v100
	s_mov_b64 exec, s[36:37]
	v_lshl_or_b32 v166, v103, 16, v102
	v_lshl_or_b32 v167, v105, 16, v104
	s_mov_b64 exec, -1
	ds_read_u16 v98, v192 offset:3584
	ds_read_u16 v99, v192 offset:3600
	ds_read_u16 v100, v192 offset:3616
	ds_read_u16 v101, v192 offset:3632
	ds_read_u16 v102, v193 offset:896
	ds_read_u16 v103, v193 offset:912
	ds_read_u16 v104, v193 offset:928
	ds_read_u16 v105, v193 offset:944
	s_waitcnt lgkmcnt(8)
	v_lshl_or_b32 v168, v83, 16, v82
	v_lshl_or_b32 v169, v85, 16, v84
	s_mov_b64 exec, s[36:37]
	v_lshl_or_b32 v170, v91, 16, v90
	v_lshl_or_b32 v171, v93, 16, v92
	s_mov_b64 exec, -1
	ds_read_u16 v82, v192 offset:4096
	ds_read_u16 v83, v192 offset:4112
	ds_read_u16 v84, v192 offset:4128
	ds_read_u16 v85, v192 offset:4144
	ds_read_u16 v90, v193 offset:1024
	ds_read_u16 v91, v193 offset:1040
	ds_read_u16 v92, v193 offset:1056
	ds_read_u16 v93, v193 offset:1072
	s_waitcnt lgkmcnt(8)
	v_lshl_or_b32 v172, v99, 16, v98
	v_lshl_or_b32 v173, v101, 16, v100
	s_mov_b64 exec, s[36:37]
	v_lshl_or_b32 v174, v103, 16, v102
	v_lshl_or_b32 v175, v105, 16, v104
	s_mov_b64 exec, -1
	ds_read_u16 v98, v192 offset:4608
	ds_read_u16 v99, v192 offset:4624
	ds_read_u16 v100, v192 offset:4640
	ds_read_u16 v101, v192 offset:4656
	ds_read_u16 v102, v193 offset:1152
	ds_read_u16 v103, v193 offset:1168
	ds_read_u16 v104, v193 offset:1184
	ds_read_u16 v105, v193 offset:1200
	s_waitcnt lgkmcnt(8)
	v_lshl_or_b32 v176, v83, 16, v82
	v_lshl_or_b32 v177, v85, 16, v84
	s_mov_b64 exec, s[36:37]
	v_lshl_or_b32 v178, v91, 16, v90
	v_lshl_or_b32 v179, v93, 16, v92
	s_mov_b64 exec, -1
	ds_read_u16 v82, v192 offset:5120
	ds_read_u16 v83, v192 offset:5136
	ds_read_u16 v84, v192 offset:5152
	ds_read_u16 v85, v192 offset:5168
	ds_read_u16 v90, v193 offset:1280
	ds_read_u16 v91, v193 offset:1296
	ds_read_u16 v92, v193 offset:1312
	ds_read_u16 v93, v193 offset:1328
	s_waitcnt lgkmcnt(8)
	v_lshl_or_b32 v180, v99, 16, v98
	v_lshl_or_b32 v181, v101, 16, v100
	s_mov_b64 exec, s[36:37]
	v_lshl_or_b32 v182, v103, 16, v102
	v_lshl_or_b32 v183, v105, 16, v104
	s_mov_b64 exec, -1
	ds_read_u16 v98, v192 offset:5632
	ds_read_u16 v99, v192 offset:5648
	ds_read_u16 v100, v192 offset:5664
	ds_read_u16 v101, v192 offset:5680
	ds_read_u16 v102, v193 offset:1408
	ds_read_u16 v103, v193 offset:1424
	ds_read_u16 v104, v193 offset:1440
	ds_read_u16 v105, v193 offset:1456
	s_waitcnt lgkmcnt(8)
	v_lshl_or_b32 v184, v83, 16, v82
	v_lshl_or_b32 v185, v85, 16, v84
	s_mov_b64 exec, s[36:37]
	v_lshl_or_b32 v186, v91, 16, v90
	v_lshl_or_b32 v187, v93, 16, v92
	s_mov_b64 exec, -1
	ds_read_u16 v82, v192 offset:6144
	ds_read_u16 v83, v192 offset:6160
	ds_read_u16 v84, v192 offset:6176
	ds_read_u16 v85, v192 offset:6192
	ds_read_u16 v90, v193 offset:1536
	ds_read_u16 v91, v193 offset:1552
	ds_read_u16 v92, v193 offset:1568
	ds_read_u16 v93, v193 offset:1584
	s_waitcnt lgkmcnt(8)
	v_lshl_or_b32 v188, v99, 16, v98
	v_lshl_or_b32 v189, v101, 16, v100
	s_mov_b64 exec, s[36:37]
	v_lshl_or_b32 v190, v103, 16, v102
	v_lshl_or_b32 v191, v105, 16, v104
	s_mov_b64 exec, -1
	ds_read_u16 v98, v192 offset:6656
	ds_read_u16 v99, v192 offset:6672
	ds_read_u16 v100, v192 offset:6688
	ds_read_u16 v101, v192 offset:6704
	ds_read_u16 v102, v193 offset:1664
	ds_read_u16 v103, v193 offset:1680
	ds_read_u16 v104, v193 offset:1696
	ds_read_u16 v105, v193 offset:1712
	s_waitcnt lgkmcnt(8)
	v_lshl_or_b32 v232, v83, 16, v82
	v_lshl_or_b32 v233, v85, 16, v84
	s_mov_b64 exec, s[36:37]
	v_lshl_or_b32 v234, v91, 16, v90
	v_lshl_or_b32 v235, v93, 16, v92
	s_mov_b64 exec, -1
	ds_read_u16 v82, v192 offset:7168
	ds_read_u16 v83, v192 offset:7184
	ds_read_u16 v84, v192 offset:7200
	ds_read_u16 v85, v192 offset:7216
	ds_read_u16 v90, v193 offset:1792
	ds_read_u16 v91, v193 offset:1808
	ds_read_u16 v92, v193 offset:1824
	ds_read_u16 v93, v193 offset:1840
	s_waitcnt lgkmcnt(8)
	v_lshl_or_b32 v236, v99, 16, v98
	v_lshl_or_b32 v237, v101, 16, v100
	s_mov_b64 exec, s[36:37]
	v_lshl_or_b32 v238, v103, 16, v102
	v_lshl_or_b32 v239, v105, 16, v104
	s_mov_b64 exec, -1
	ds_read_u16 v98, v192 offset:7680
	ds_read_u16 v99, v192 offset:7696
	ds_read_u16 v100, v192 offset:7712
	ds_read_u16 v101, v192 offset:7728
	ds_read_u16 v102, v193 offset:1920
	ds_read_u16 v103, v193 offset:1936
	ds_read_u16 v104, v193 offset:1952
	ds_read_u16 v105, v193 offset:1968
	s_waitcnt lgkmcnt(8)
	v_lshl_or_b32 v240, v83, 16, v82
	v_lshl_or_b32 v241, v85, 16, v84
	s_mov_b64 exec, s[36:37]
	v_lshl_or_b32 v242, v91, 16, v90
	v_lshl_or_b32 v243, v93, 16, v92
	s_mov_b64 exec, -1
	s_waitcnt lgkmcnt(0)
	v_lshl_or_b32 v244, v99, 16, v98
	v_lshl_or_b32 v245, v101, 16, v100
	s_mov_b64 exec, s[36:37]
	v_lshl_or_b32 v246, v103, 16, v102
	v_lshl_or_b32 v247, v105, 16, v104
	s_mov_b64 exec, -1
	s_waitcnt lgkmcnt(0)
	s_mov_b64 exec, s[38:39]
	v_cvt_pk_bf16_f32 v66, v2, v195
	v_cvt_pk_bf16_f32 v74, v3, v195
	v_lshlrev_b32_e32 v67, 16, v66
	v_lshlrev_b32_e32 v75, 16, v74
	v_sub_f32_e32 v2, v2, v67
	v_sub_f32_e32 v3, v3, v75
	v_cvt_pk_bf16_f32 v68, v2, v195
	v_cvt_pk_bf16_f32 v76, v3, v195
	v_lshlrev_b32_e32 v69, 16, v68
	v_lshlrev_b32_e32 v77, 16, v76
	v_sub_f32_e32 v2, v2, v69
	v_sub_f32_e32 v3, v3, v77
	v_cvt_pk_bf16_f32 v147, v2, v195
	v_cvt_pk_bf16_f32 v151, v3, v195
	v_cvt_pk_bf16_f32 v146, v67, v69
	v_cvt_pk_bf16_f32 v150, v75, v77
	v_cvt_pk_bf16_f32 v66, v4, v195
	v_cvt_pk_bf16_f32 v74, v5, v195
	v_lshlrev_b32_e32 v67, 16, v66
	v_lshlrev_b32_e32 v75, 16, v74
	v_sub_f32_e32 v4, v4, v67
	v_sub_f32_e32 v5, v5, v75
	v_cvt_pk_bf16_f32 v68, v4, v195
	v_cvt_pk_bf16_f32 v76, v5, v195
	v_lshlrev_b32_e32 v69, 16, v68
	v_lshlrev_b32_e32 v77, 16, v76
	v_sub_f32_e32 v4, v4, v69
	v_sub_f32_e32 v5, v5, v77
	v_cvt_pk_bf16_f32 v155, v4, v195
	v_cvt_pk_bf16_f32 v159, v5, v195
	v_cvt_pk_bf16_f32 v154, v67, v69
	v_cvt_pk_bf16_f32 v158, v75, v77
	v_cvt_pk_bf16_f32 v66, v6, v195
	v_cvt_pk_bf16_f32 v74, v7, v195
	v_lshlrev_b32_e32 v67, 16, v66
	v_lshlrev_b32_e32 v75, 16, v74
	v_sub_f32_e32 v6, v6, v67
	v_sub_f32_e32 v7, v7, v75
	v_cvt_pk_bf16_f32 v68, v6, v195
	v_cvt_pk_bf16_f32 v76, v7, v195
	v_lshlrev_b32_e32 v69, 16, v68
	v_lshlrev_b32_e32 v77, 16, v76
	v_sub_f32_e32 v6, v6, v69
	v_sub_f32_e32 v7, v7, v77
	v_cvt_pk_bf16_f32 v163, v6, v195
	v_cvt_pk_bf16_f32 v167, v7, v195
	v_cvt_pk_bf16_f32 v162, v67, v69
	v_cvt_pk_bf16_f32 v166, v75, v77
	v_cvt_pk_bf16_f32 v66, v8, v195
	v_cvt_pk_bf16_f32 v74, v9, v195
	v_lshlrev_b32_e32 v67, 16, v66
	v_lshlrev_b32_e32 v75, 16, v74
	v_sub_f32_e32 v8, v8, v67
	v_sub_f32_e32 v9, v9, v75
	v_cvt_pk_bf16_f32 v68, v8, v195
	v_cvt_pk_bf16_f32 v76, v9, v195
	v_lshlrev_b32_e32 v69, 16, v68
	v_lshlrev_b32_e32 v77, 16, v76
	v_sub_f32_e32 v8, v8, v69
	v_sub_f32_e32 v9, v9, v77
	v_cvt_pk_bf16_f32 v171, v8, v195
	v_cvt_pk_bf16_f32 v175, v9, v195
	v_cvt_pk_bf16_f32 v170, v67, v69
	v_cvt_pk_bf16_f32 v174, v75, v77
	v_cvt_pk_bf16_f32 v66, v50, v195
	v_cvt_pk_bf16_f32 v74, v51, v195
	v_lshlrev_b32_e32 v67, 16, v66
	v_lshlrev_b32_e32 v75, 16, v74
	v_sub_f32_e32 v50, v50, v67
	v_sub_f32_e32 v51, v51, v75
	v_cvt_pk_bf16_f32 v68, v50, v195
	v_cvt_pk_bf16_f32 v76, v51, v195
	v_lshlrev_b32_e32 v69, 16, v68
	v_lshlrev_b32_e32 v77, 16, v76
	v_sub_f32_e32 v50, v50, v69
	v_sub_f32_e32 v51, v51, v77
	v_cvt_pk_bf16_f32 v179, v50, v195
	v_cvt_pk_bf16_f32 v183, v51, v195
	v_cvt_pk_bf16_f32 v178, v67, v69
	v_cvt_pk_bf16_f32 v182, v75, v77
	v_cvt_pk_bf16_f32 v66, v52, v195
	v_cvt_pk_bf16_f32 v74, v53, v195
	v_lshlrev_b32_e32 v67, 16, v66
	v_lshlrev_b32_e32 v75, 16, v74
	v_sub_f32_e32 v52, v52, v67
	v_sub_f32_e32 v53, v53, v75
	v_cvt_pk_bf16_f32 v68, v52, v195
	v_cvt_pk_bf16_f32 v76, v53, v195
	v_lshlrev_b32_e32 v69, 16, v68
	v_lshlrev_b32_e32 v77, 16, v76
	v_sub_f32_e32 v52, v52, v69
	v_sub_f32_e32 v53, v53, v77
	v_cvt_pk_bf16_f32 v187, v52, v195
	v_cvt_pk_bf16_f32 v191, v53, v195
	v_cvt_pk_bf16_f32 v186, v67, v69
	v_cvt_pk_bf16_f32 v190, v75, v77
	v_cvt_pk_bf16_f32 v66, v58, v195
	v_cvt_pk_bf16_f32 v74, v59, v195
	v_lshlrev_b32_e32 v67, 16, v66
	v_lshlrev_b32_e32 v75, 16, v74
	v_sub_f32_e32 v58, v58, v67
	v_sub_f32_e32 v59, v59, v75
	v_cvt_pk_bf16_f32 v68, v58, v195
	v_cvt_pk_bf16_f32 v76, v59, v195
	v_lshlrev_b32_e32 v69, 16, v68
	v_lshlrev_b32_e32 v77, 16, v76
	v_sub_f32_e32 v58, v58, v69
	v_sub_f32_e32 v59, v59, v77
	v_cvt_pk_bf16_f32 v235, v58, v195
	v_cvt_pk_bf16_f32 v239, v59, v195
	v_cvt_pk_bf16_f32 v234, v67, v69
	v_cvt_pk_bf16_f32 v238, v75, v77
	v_cvt_pk_bf16_f32 v66, v60, v195
	v_cvt_pk_bf16_f32 v74, v61, v195
	v_lshlrev_b32_e32 v67, 16, v66
	v_lshlrev_b32_e32 v75, 16, v74
	v_sub_f32_e32 v60, v60, v67
	v_sub_f32_e32 v61, v61, v75
	v_cvt_pk_bf16_f32 v68, v60, v195
	v_cvt_pk_bf16_f32 v76, v61, v195
	v_lshlrev_b32_e32 v69, 16, v68
	v_lshlrev_b32_e32 v77, 16, v76
	v_sub_f32_e32 v60, v60, v69
	v_sub_f32_e32 v61, v61, v77
	v_cvt_pk_bf16_f32 v243, v60, v195
	v_cvt_pk_bf16_f32 v247, v61, v195
	v_cvt_pk_bf16_f32 v242, v67, v69
	v_cvt_pk_bf16_f32 v246, v75, v77
	s_mov_b64 exec, -1
	v_lshlrev_b32_e32 v192, 3, v142
	v_and_b32_e32 v192, 56, v192
	v_lshl_or_b32 v193, v192, 8, v204
	v_lshl_or_b32 v192, v192, 10, v198
	s_nop 4
	v_mfma_f32_16x16x32_bf16 v[2:5], v[26:29], v[42:45], v[18:21]
	s_nop 1
	ds_read_b128 v[58:61], v192
	ds_read_b128 v[110:113], v193
	ds_read_b128 v[50:53], v192 offset:1024
	ds_read_b128 v[118:121], v193 offset:256
	ds_read_b128 v[66:69], v192 offset:2048
	ds_read_b128 v[126:129], v193 offset:512
	ds_read_b128 v[74:77], v192 offset:3072
	ds_read_b128 v[134:137], v193 offset:768
	ds_read_b128 v[82:85], v192 offset:4096
	ds_read_b128 v[138:141], v193 offset:1024
	ds_read_b128 v[90:93], v192 offset:5120
	ds_read_b128 v[18:21], v193 offset:1280
	ds_read_b128 v[98:101], v192 offset:6144
	ds_read_b128 v[26:29], v193 offset:1536
	ds_read_b128 v[102:105], v192 offset:7168
	ds_read_b128 v[42:45], v193 offset:1792
	s_waitcnt vmcnt(15)
	v_cvt_pk_bf16_f32 v6, v10, v11
	v_cvt_pk_bf16_f32 v7, v12, v13
	ds_write_b64 v212, v[6:7]
	s_waitcnt vmcnt(14)
	v_cvt_pk_bf16_f32 v6, v14, v15
	v_cvt_pk_bf16_f32 v7, v16, v17
	ds_write_b64 v211, v[6:7] offset:512
	s_waitcnt vmcnt(13)
	v_cvt_pk_bf16_f32 v6, v22, v23
	v_cvt_pk_bf16_f32 v7, v24, v25
	ds_write_b64 v210, v[6:7] offset:1024
	s_waitcnt vmcnt(12)
	v_cvt_pk_bf16_f32 v6, v30, v31
	v_cvt_pk_bf16_f32 v7, v32, v33
	ds_write_b64 v209, v[6:7] offset:1536
	s_waitcnt vmcnt(11)
	v_cvt_pk_bf16_f32 v6, v38, v39
	v_cvt_pk_bf16_f32 v7, v40, v41
	ds_write_b64 v208, v[6:7] offset:2048
	s_waitcnt vmcnt(10)
	v_cvt_pk_bf16_f32 v6, v46, v47
	v_cvt_pk_bf16_f32 v7, v48, v49
	ds_write_b64 v207, v[6:7] offset:2560
	s_waitcnt vmcnt(9)
	v_cvt_pk_bf16_f32 v6, v54, v55
	v_cvt_pk_bf16_f32 v7, v56, v57
	ds_write_b64 v206, v[6:7] offset:3072
	s_waitcnt vmcnt(8)
	v_cvt_pk_bf16_f32 v6, v62, v63
	v_cvt_pk_bf16_f32 v7, v64, v65
	ds_write_b64 v205, v[6:7] offset:3584
	s_waitcnt vmcnt(7)
	v_cvt_pk_bf16_f32 v6, v70, v71
	v_cvt_pk_bf16_f32 v7, v72, v73
	ds_write_b64 v231, v[6:7] offset:4096
	s_waitcnt vmcnt(6)
	v_cvt_pk_bf16_f32 v6, v78, v79
	v_cvt_pk_bf16_f32 v7, v80, v81
	ds_write_b64 v230, v[6:7] offset:4608
	s_waitcnt vmcnt(5)
	v_cvt_pk_bf16_f32 v6, v86, v87
	v_cvt_pk_bf16_f32 v7, v88, v89
	ds_write_b64 v229, v[6:7] offset:5120
	s_waitcnt vmcnt(4)
	v_cvt_pk_bf16_f32 v6, v94, v95
	v_cvt_pk_bf16_f32 v7, v96, v97
	ds_write_b64 v228, v[6:7] offset:5632
	s_waitcnt vmcnt(3)
	v_cvt_pk_bf16_f32 v6, v106, v107
	v_cvt_pk_bf16_f32 v7, v108, v109
	ds_write_b64 v227, v[6:7] offset:6144
	s_waitcnt vmcnt(2)
	v_cvt_pk_bf16_f32 v6, v114, v115
	v_cvt_pk_bf16_f32 v7, v116, v117
	ds_write_b64 v226, v[6:7] offset:6656
	s_waitcnt vmcnt(1)
	v_cvt_pk_bf16_f32 v6, v122, v123
	v_cvt_pk_bf16_f32 v7, v124, v125
	ds_write_b64 v225, v[6:7] offset:7168
	s_waitcnt vmcnt(0)
	v_cvt_pk_bf16_f32 v6, v130, v131
	v_cvt_pk_bf16_f32 v7, v132, v133
	ds_write_b64 v224, v[6:7] offset:7680
	ds_read_b128 v[54:57], v223
	ds_read_b128 v[62:65], v222
	ds_read_b128 v[10:13], v221
	ds_read_b128 v[14:17], v219
	ds_read_b128 v[22:25], v218
	ds_read_b128 v[30:33], v217
	ds_read_b128 v[38:41], v216
	ds_read_b128 v[46:49], v213
	s_waitcnt lgkmcnt(7)
	v_mfma_f32_16x16x32_bf16 v[34:37], v[58:61], v[54:57], v[34:37]
	v_mfma_f32_16x16x32_bf16 v[2:5], v[110:113], v[54:57], v[2:5]
	s_waitcnt lgkmcnt(6)
	v_mfma_f32_16x16x32_bf16 v[34:37], v[50:53], v[62:65], v[34:37]
	v_mfma_f32_16x16x32_bf16 v[2:5], v[118:121], v[62:65], v[2:5]
	s_waitcnt lgkmcnt(5)
	v_mfma_f32_16x16x32_bf16 v[34:37], v[66:69], v[10:13], v[34:37]
	v_mfma_f32_16x16x32_bf16 v[2:5], v[126:129], v[10:13], v[2:5]
	s_waitcnt lgkmcnt(4)
	v_mfma_f32_16x16x32_bf16 v[34:37], v[74:77], v[14:17], v[34:37]
	v_mfma_f32_16x16x32_bf16 v[2:5], v[134:137], v[14:17], v[2:5]
	s_waitcnt lgkmcnt(3)
	v_mfma_f32_16x16x32_bf16 v[34:37], v[82:85], v[22:25], v[34:37]
	v_mfma_f32_16x16x32_bf16 v[2:5], v[138:141], v[22:25], v[2:5]
	s_waitcnt lgkmcnt(2)
	v_mfma_f32_16x16x32_bf16 v[34:37], v[90:93], v[30:33], v[34:37]
	v_mfma_f32_16x16x32_bf16 v[2:5], v[18:21], v[30:33], v[2:5]
	s_waitcnt lgkmcnt(1)
	v_mfma_f32_16x16x32_bf16 v[34:37], v[98:101], v[38:41], v[34:37]
	v_mfma_f32_16x16x32_bf16 v[2:5], v[26:29], v[38:41], v[2:5]
	s_waitcnt lgkmcnt(0)
	v_mfma_f32_16x16x32_bf16 v[56:59], v[102:105], v[46:49], v[34:37]
	v_mfma_f32_16x16x32_bf16 v[60:63], v[42:45], v[46:49], v[2:5]
	v_add_u32_e32 v76, 0x24800, v196
	s_waitcnt lgkmcnt(0)
	v_cmp_gt_u32_e64 s[0:1], 16, v1
	v_cmp_lt_u32_e32 vcc, 15, v1
	s_waitcnt lgkmcnt(0)
	s_nop 2
	v_max_f32_e32 v2, v59, v59
	v_max_f32_e32 v3, v58, v58
	s_waitcnt lgkmcnt(0)
	v_max_f32_e32 v2, v3, v2
	s_nop 0
	s_nop 0
	s_nop 0
	s_waitcnt lgkmcnt(0)
	s_nop 0
	s_nop 0
	s_and_saveexec_b64 s[4:5], vcc
	s_xor_b64 s[4:5], exec, s[4:5]
	s_or_saveexec_b64 s[4:5], s[4:5]
	v_max3_f32 v53, v56, v57, v2
	s_xor_b64 exec, exec, s[4:5]
	v_max_f32_e32 v2, v61, v61
	v_max_f32_e32 v3, v60, v60
	v_max_f32_e32 v2, v3, v2
	v_max_f32_e32 v3, v63, v63
	v_max_f32_e32 v4, v62, v62
	v_max_f32_e32 v3, v4, v3
	v_max3_f32 v53, v53, v2, v3
	s_or_b64 exec, exec, s[4:5]
	v_cmp_eq_u32_e64 s[4:5], 1, v201
	v_max_f32_e32 v53, v53, v53
	v_mov_b32_e32 v68, v53
	s_nop 1
	v_permlane16_swap_b32_e32 v53, v68
	v_max_f32_e32 v68, v53, v68
	v_mov_b32_e32 v55, v68
	s_nop 1
	v_permlane32_swap_b32_e32 v68, v55
	v_max_f32_e32 v68, v68, v55
	v_sub_f32_e32 v55, v56, v68
	v_mul_f32_e32 v55, 0x3fb8aa3b, v55
	v_exp_f32_e32 v70, v55
	v_sub_f32_e32 v55, v57, v68
	v_sub_f32_e32 v57, v59, v68
	v_mul_f32_e32 v57, 0x3fb8aa3b, v57
	v_mul_f32_e32 v55, 0x3fb8aa3b, v55
	v_exp_f32_e32 v59, v57
	v_sub_f32_e32 v57, v60, v68
	v_exp_f32_e32 v71, v55
	v_sub_f32_e32 v55, v58, v68
	v_mul_f32_e32 v57, 0x3fb8aa3b, v57
	v_sub_f32_e32 v58, v61, v68
	v_exp_f32_e32 v57, v57
	v_mul_f32_e32 v58, 0x3fb8aa3b, v58
	v_exp_f32_e32 v58, v58
	v_mul_f32_e32 v55, 0x3fb8aa3b, v55
	v_exp_f32_e32 v72, v55
	v_cndmask_b32_e64 v60, 0, v57, s[0:1]
	v_sub_f32_e32 v57, v62, v68
	v_add_f32_e32 v56, 0, v70
	v_cndmask_b32_e64 v61, 0, v58, s[0:1]
	v_mul_f32_e32 v57, 0x3fb8aa3b, v57
	v_sub_f32_e32 v58, v63, v68
	v_add_f32_e32 v56, v56, v71
	v_exp_f32_e32 v57, v57
	v_mul_f32_e32 v58, 0x3fb8aa3b, v58
	v_add_f32_e32 v56, v56, v72
	v_exp_f32_e32 v58, v58
	v_add_f32_e32 v56, v56, v59
	v_add_f32_e32 v56, v56, v60
	v_add_f32_e32 v56, v56, v61
	v_cndmask_b32_e64 v62, 0, v57, s[0:1]
	v_add_f32_e32 v56, v56, v62
	v_cndmask_b32_e64 v63, 0, v58, s[0:1]
	v_add_f32_e32 v57, v56, v63
	v_mov_b32_e32 v58, v57
	s_nop 1
	v_permlane16_swap_b32_e32 v57, v58
	v_add_f32_e32 v58, v57, v58
	v_mov_b32_e32 v68, v58
	s_nop 1
	v_permlane32_swap_b32_e32 v58, v68
	v_add_f32_e32 v68, v58, v68
	v_div_scale_f32 v69, s[6:7], v68, v68, 1.0
	v_rcp_f32_e32 v73, v69
	s_nop 0
	v_fma_f32 v75, -v69, v73, 1.0
	v_fmac_f32_e32 v73, v75, v73
	v_div_scale_f32 v75, vcc, 1.0, v68, 1.0
	v_mul_f32_e32 v92, v75, v73
	v_fma_f32 v93, -v69, v92, v75
	v_fmac_f32_e32 v92, v93, v73
	v_fma_f32 v69, -v69, v92, v75
	v_div_fmas_f32 v69, v69, v73, v92
	v_div_fixup_f32 v68, v69, v68, 1.0
	v_mul_f32_e32 v69, v68, v70
	v_mov_b32_e32 v75, 0xbb23d70a
	v_mov_b32_e32 v73, 0x3b23d70a
	v_fmaak_f32 v92, v68, v70, 0xbb23d70a
	v_fmaak_f32 v70, v68, v70, 0x3b23d70a
	v_cmp_lt_f32_e32 vcc, v69, v75
	v_fmaak_f32 v93, v68, v60, 0xbb23d70a
	s_nop 0
	v_cndmask_b32_e32 v70, 0, v70, vcc
	v_cmp_gt_f32_e32 vcc, v69, v73
	s_nop 1
	v_cndmask_b32_e32 v69, v70, v92, vcc
	v_mul_f32_e32 v92, v68, v60
	v_fmaak_f32 v60, v68, v60, 0x3b23d70a
	v_cmp_lt_f32_e32 vcc, v92, v75
	v_max_f32_e32 v70, 0xf149f2ca, v69
	s_nop 0
	v_cndmask_b32_e32 v60, 0, v60, vcc
	v_cmp_gt_f32_e32 vcc, v92, v73
	s_nop 1
	v_cndmask_b32_e32 v92, v60, v93, vcc
	v_max_f32_e32 v60, v70, v92
	v_cndmask_b32_e64 v60, v70, v60, s[0:1]
	v_mul_f32_e32 v70, v68, v71
	v_fmaak_f32 v93, v68, v71, 0xbb23d70a
	v_fmaak_f32 v71, v68, v71, 0x3b23d70a
	v_cmp_lt_f32_e32 vcc, v70, v75
	s_nop 1
	v_cndmask_b32_e32 v71, 0, v71, vcc
	v_cmp_gt_f32_e32 vcc, v70, v73
	s_nop 1
	v_cndmask_b32_e32 v70, v71, v93, vcc
	v_mul_f32_e32 v71, v68, v61
	v_fmaak_f32 v93, v68, v61, 0xbb23d70a
	v_fmaak_f32 v61, v68, v61, 0x3b23d70a
	v_cmp_lt_f32_e32 vcc, v71, v75
	v_max_f32_e32 v60, v60, v70
	s_nop 0
	v_cndmask_b32_e32 v61, 0, v61, vcc
	v_cmp_gt_f32_e32 vcc, v71, v73
	s_nop 1
	v_cndmask_b32_e32 v71, v61, v93, vcc
	v_max_f32_e32 v61, v60, v71
	v_cndmask_b32_e64 v60, v60, v61, s[0:1]
	v_mul_f32_e32 v61, v68, v72
	v_fmaak_f32 v93, v68, v72, 0xbb23d70a
	v_fmaak_f32 v72, v68, v72, 0x3b23d70a
	v_cmp_lt_f32_e32 vcc, v61, v75
	s_nop 1
	v_cndmask_b32_e32 v72, 0, v72, vcc
	v_cmp_gt_f32_e32 vcc, v61, v73
	v_mul_f32_e32 v61, v68, v62
	s_nop 0
	v_cndmask_b32_e32 v72, v72, v93, vcc
	v_fmaak_f32 v93, v68, v62, 0xbb23d70a
	v_fmaak_f32 v62, v68, v62, 0x3b23d70a
	v_cmp_lt_f32_e32 vcc, v61, v75
	v_max_f32_e32 v60, v60, v72
	s_nop 0
	v_cndmask_b32_e32 v62, 0, v62, vcc
	v_cmp_gt_f32_e32 vcc, v61, v73
	s_nop 1
	v_cndmask_b32_e32 v62, v62, v93, vcc
	v_max_f32_e32 v61, v60, v62
	v_cndmask_b32_e64 v60, v60, v61, s[0:1]
	v_mul_f32_e32 v61, v68, v59
	v_fmaak_f32 v93, v68, v59, 0xbb23d70a
	v_fmaak_f32 v59, v68, v59, 0x3b23d70a
	v_cmp_lt_f32_e32 vcc, v61, v75
	s_nop 1
	v_cndmask_b32_e32 v59, 0, v59, vcc
	v_cmp_gt_f32_e32 vcc, v61, v73
	s_nop 1
	v_cndmask_b32_e32 v93, v59, v93, vcc
	v_max_f32_e32 v59, v60, v93
	v_mul_f32_e32 v60, v68, v63
	v_cmp_gt_f32_e32 vcc, v60, v73
	v_fmac_f32_e32 v73, v68, v63
	v_cmp_lt_f32_e64 s[6:7], v60, v75
	v_fmac_f32_e32 v75, v68, v63
	s_nop 0
	v_cndmask_b32_e64 v60, 0, v73, s[6:7]
	v_cndmask_b32_e32 v63, v60, v75, vcc
	v_max_f32_e32 v60, v59, v63
	v_cndmask_b32_e64 v60, v59, v60, s[0:1]
	v_mov_b32_e32 v61, v60
	s_nop 1
	v_permlane16_swap_b32_e32 v60, v61
	v_max_f32_e32 v61, v60, v61
	v_mov_b32_e32 v74, v61
	s_nop 1
	v_permlane32_swap_b32_e32 v61, v74
	v_max_f32_e32 v74, v61, v74
	v_sub_f32_e32 v61, v69, v74
	v_mul_f32_e32 v61, 0x3fb8aa3b, v61
	v_exp_f32_e32 v69, v61
	v_sub_f32_e32 v61, v92, v74
	v_mul_f32_e32 v61, 0x3fb8aa3b, v61
	v_exp_f32_e32 v75, v61
	v_sub_f32_e32 v70, v70, v74
	v_sub_f32_e32 v71, v71, v74
	v_mul_f32_e32 v70, 0x3fb8aa3b, v70
	v_mul_f32_e32 v71, 0x3fb8aa3b, v71
	v_exp_f32_e32 v70, v70
	v_exp_f32_e32 v71, v71
	v_sub_f32_e32 v72, v72, v74
	v_sub_f32_e32 v62, v62, v74
	v_mul_f32_e32 v72, 0x3fb8aa3b, v72
	v_mul_f32_e32 v62, 0x3fb8aa3b, v62
	v_add_f32_e32 v73, 0, v69
	v_cndmask_b32_e64 v75, 0, v75, s[0:1]
	v_exp_f32_e32 v72, v72
	v_exp_f32_e32 v62, v62
	v_sub_f32_e32 v84, v93, v74
	v_sub_f32_e32 v63, v63, v74
	v_add_f32_e32 v73, v73, v75
	v_mul_f32_e32 v84, 0x3fb8aa3b, v84
	v_mul_f32_e32 v63, 0x3fb8aa3b, v63
	v_add_f32_e32 v73, v73, v70
	v_cndmask_b32_e64 v71, 0, v71, s[0:1]
	v_exp_f32_e32 v84, v84
	v_exp_f32_e32 v63, v63
	v_add_f32_e32 v73, v73, v71
	v_add_f32_e32 v73, v73, v72
	v_cndmask_b32_e64 v74, 0, v62, s[0:1]
	v_add_f32_e32 v62, v73, v74
	v_add_f32_e32 v62, v62, v84
	v_cndmask_b32_e64 v73, 0, v63, s[0:1]
	v_add_f32_e32 v85, v62, v73
	v_mov_b32_e32 v66, v85
	s_nop 1
	v_permlane16_swap_b32_e32 v85, v66
	v_add_f32_e32 v66, v85, v66
	v_mov_b32_e32 v67, v66
	s_nop 1
	v_permlane32_swap_b32_e32 v66, v67
	v_add_f32_e32 v66, v66, v67
	v_div_scale_f32 v67, s[6:7], v66, v66, 1.0
	v_rcp_f32_e32 v78, v67
	s_nop 0
	v_fma_f32 v68, -v67, v78, 1.0
	v_fmac_f32_e32 v78, v68, v78
	v_div_scale_f32 v68, vcc, 1.0, v66, 1.0
	v_mul_f32_e32 v77, v68, v78
	v_fma_f32 v79, -v67, v77, v68
	v_fmac_f32_e32 v77, v79, v78
	v_fma_f32 v67, -v67, v77, v68
	v_div_fmas_f32 v67, v67, v78, v77
	v_div_fixup_f32 v66, v67, v66, 1.0
	v_mov_b32_e32 v67, 0xbd4ccccd
	v_fmaak_f32 v68, v66, v69, 0xbd4ccccd
	v_fmaak_f32 v69, v66, v70, 0xbd4ccccd
	v_fmaak_f32 v70, v66, v72, 0xbd4ccccd
	v_fmaak_f32 v75, v66, v75, 0xbd4ccccd
	v_fmaak_f32 v71, v66, v71, 0xbd4ccccd
	v_fmaak_f32 v74, v66, v74, 0xbd4ccccd
	v_mul_f32_e32 v70, 0x4038aa3b, v70
	v_fmaak_f32 v72, v66, v84, 0xbd4ccccd
	v_mul_f32_e32 v75, 0x4038aa3b, v75
	v_mul_f32_e32 v71, 0x4038aa3b, v71
	v_mul_f32_e32 v74, 0x4038aa3b, v74
	v_fmac_f32_e32 v67, v66, v73
	v_mul_f32_e32 v68, 0x4038aa3b, v68
	v_mul_f32_e32 v69, 0x4038aa3b, v69
	v_mul_f32_e32 v72, 0x4038aa3b, v72
	v_cndmask_b32_e64 v75, 0, v75, s[0:1]
	v_cndmask_b32_e64 v71, 0, v71, s[0:1]
	v_cndmask_b32_e64 v74, 0, v74, s[0:1]
	v_mul_f32_e32 v66, 0x4038aa3b, v67
	v_cvt_pk_bf16_f32 v67, v70, v72
	v_add_u32_e32 v70, v76, v198
	v_cndmask_b32_e64 v73, 0, v66, s[0:1]
	v_cndmask_b32_e64 v74, v74, 1.0, s[4:5]
	v_cndmask_b32_e64 v75, v75, 1.0, s[4:5]
	v_cndmask_b32_e64 v71, v71, 1.0, s[4:5]
	v_cvt_pk_bf16_f32 v66, v68, v69
	v_cvt_pk_bf16_f32 v68, v75, v71
	v_cvt_pk_bf16_f32 v69, v74, v73
	ds_write_b128 v70, v[66:69]
	s_movk_i32 s0, 0x210
	v_and_b32_e32 v67, 48, v0
	v_lshrrev_b32_e32 v0, 5, v1
	v_mad_u32_u24 v66, v197, s0, v199
	v_mad_u32_u24 v68, v0, s0, v199
	s_and_b32 s0, s2, 7
	s_lshl_b32 s0, s0, 22
	s_lshl_b32 s1, s3, 17
	v_lshlrev_b32_e32 v1, 13, v0
	s_add_i32 s0, s0, s1
	v_and_b32_e32 v69, 0x1f0, v194
	v_or3_b32 v1, s0, v1, v196
	s_mov_b32 s12, 0
	s_mov_b32 s11, 0x20000
	s_brev_b32 s10, 8
	s_and_b32 s9, s9, 0xffff
	v_or_b32_e32 v0, 0x24800, v198
	v_add_u32_e32 v1, v1, v69
	v_add_u32_e32 v106, v66, v67
	v_add_u32_e32 v107, v68, v69
	s_waitcnt lgkmcnt(0)
	s_barrier
